# 8-phase GEMM K-loops without the per-segment s_setprio 1/0 toggling around the MFMA blocks (all waves at priority 0 in the K-loops)
# speedup vs baseline: 1.0005x; 1.0005x over previous
.LBB0_191:
	ds_read_b128 v[134:137], v150
	ds_read_b128 v[156:159], v150 offset:1024
	ds_read_b128 v[160:163], v150 offset:2048
	ds_read_b128 v[164:167], v150 offset:3072
	ds_read_b128 v[168:171], v151
	ds_read_b128 v[172:175], v151 offset:1024
	ds_read_b128 v[176:179], v151 offset:2048
	ds_read_b128 v[180:183], v151 offset:3072
	s_add_i32 s67, s8, 0xfff40080
	s_cmp_eq_u32 s65, 28
	s_cselect_b32 s67, s63, s67
	s_cselect_b32 s69, s64, s9
	s_add_i32 s68, s67, 0x80
	s_add_i32 s70, s8, 0xfffc0000
	s_mov_b32 m0, s55
	ds_read_b128 v[184:187], v152
	ds_read_b128 v[188:191], v152 offset:1024
	ds_read_b128 v[192:195], v152 offset:2048
	ds_read_b128 v[196:199], v152 offset:3072
	ds_read_b128 v[200:203], v152 offset:4096
	ds_read_b128 v[204:207], v152 offset:5120
	ds_read_b128 v[208:211], v152 offset:6144
	ds_read_b128 v[212:215], v152 offset:7168
	buffer_load_dwordx4 v131, s[12:15], s70 offen lds
	s_mov_b32 m0, s56
	s_nop 0
	buffer_load_dwordx4 v131, s[12:15], s8 offen lds
	s_waitcnt vmcnt(8)
	s_waitcnt lgkmcnt(0)
	s_barrier
	s_waitcnt lgkmcnt(7)
	v_mfma_f32_16x16x32_bf16 v[126:129], v[134:137], v[184:187], v[126:129]
	v_mfma_f32_16x16x32_bf16 v[122:125], v[160:163], v[184:187], v[122:125]
	s_waitcnt lgkmcnt(5)
	v_mfma_f32_16x16x32_bf16 v[118:121], v[134:137], v[192:195], v[118:121]
	v_mfma_f32_16x16x32_bf16 v[110:113], v[160:163], v[192:195], v[110:113]
	s_waitcnt lgkmcnt(3)
	v_mfma_f32_16x16x32_bf16 v[102:105], v[134:137], v[200:203], v[102:105]
	v_mfma_f32_16x16x32_bf16 v[94:97], v[160:163], v[200:203], v[94:97]
	s_waitcnt lgkmcnt(1)
	v_mfma_f32_16x16x32_bf16 v[86:89], v[134:137], v[208:211], v[86:89]
	v_mfma_f32_16x16x32_bf16 v[78:81], v[160:163], v[208:211], v[78:81]
	v_mfma_f32_16x16x32_bf16 v[126:129], v[156:159], v[188:191], v[126:129]
	v_mfma_f32_16x16x32_bf16 v[122:125], v[164:167], v[188:191], v[122:125]
	v_mfma_f32_16x16x32_bf16 v[118:121], v[156:159], v[196:199], v[118:121]
	v_mfma_f32_16x16x32_bf16 v[110:113], v[164:167], v[196:199], v[110:113]
	v_mfma_f32_16x16x32_bf16 v[102:105], v[156:159], v[204:207], v[102:105]
	v_mfma_f32_16x16x32_bf16 v[94:97], v[164:167], v[204:207], v[94:97]
	s_waitcnt lgkmcnt(0)
	v_mfma_f32_16x16x32_bf16 v[86:89], v[156:159], v[212:215], v[86:89]
	v_mfma_f32_16x16x32_bf16 v[78:81], v[164:167], v[212:215], v[78:81]
	v_mfma_f32_16x16x32_bf16 v[114:117], v[168:171], v[184:187], v[114:117]
	v_mfma_f32_16x16x32_bf16 v[106:109], v[176:179], v[184:187], v[106:109]
	v_mfma_f32_16x16x32_bf16 v[98:101], v[168:171], v[192:195], v[98:101]
	v_mfma_f32_16x16x32_bf16 v[90:93], v[176:179], v[192:195], v[90:93]
	v_mfma_f32_16x16x32_bf16 v[82:85], v[168:171], v[200:203], v[82:85]
	v_mfma_f32_16x16x32_bf16 v[74:77], v[176:179], v[200:203], v[74:77]
	v_mfma_f32_16x16x32_bf16 v[70:73], v[168:171], v[208:211], v[70:73]
	v_mfma_f32_16x16x32_bf16 v[66:69], v[176:179], v[208:211], v[66:69]
	v_mfma_f32_16x16x32_bf16 v[114:117], v[172:175], v[188:191], v[114:117]
	v_mfma_f32_16x16x32_bf16 v[106:109], v[180:183], v[188:191], v[106:109]
	v_mfma_f32_16x16x32_bf16 v[98:101], v[172:175], v[196:199], v[98:101]
	v_mfma_f32_16x16x32_bf16 v[90:93], v[180:183], v[196:199], v[90:93]
	v_mfma_f32_16x16x32_bf16 v[82:85], v[172:175], v[204:207], v[82:85]
	v_mfma_f32_16x16x32_bf16 v[74:77], v[180:183], v[204:207], v[74:77]
	v_mfma_f32_16x16x32_bf16 v[70:73], v[172:175], v[212:215], v[70:73]
	v_mfma_f32_16x16x32_bf16 v[66:69], v[180:183], v[212:215], v[66:69]
	s_barrier
	s_mov_b32 m0, s29
	ds_read_b128 v[184:187], v152 offset:16384
	ds_read_b128 v[188:191], v152 offset:17408
	ds_read_b128 v[192:195], v152 offset:18432
	ds_read_b128 v[196:199], v152 offset:19456
	ds_read_b128 v[200:203], v152 offset:20480
	ds_read_b128 v[204:207], v152 offset:21504
	ds_read_b128 v[208:211], v152 offset:22528
	ds_read_b128 v[212:215], v152 offset:23552
	buffer_load_dwordx4 v148, s[12:15], s69 offen lds
	s_add_i32 s70, s69, 0x40000
	s_mov_b32 m0, s30
	s_nop 0
	buffer_load_dwordx4 v148, s[12:15], s70 offen lds
	s_add_i32 s70, s69, 0x80000
	s_mov_b32 m0, s31
	s_nop 0
	buffer_load_dwordx4 v148, s[12:15], s70 offen lds
	s_add_i32 s70, s69, 0xc0000
	s_mov_b32 m0, s34
	s_nop 0
	buffer_load_dwordx4 v148, s[12:15], s70 offen lds
	s_mov_b32 m0, s28
	s_add_i32 s70, s67, 0x40000
	buffer_load_dwordx4 v131, s[12:15], s67 offen lds
	s_mov_b32 m0, s35
	s_nop 0
	buffer_load_dwordx4 v131, s[12:15], s70 offen lds
	s_waitcnt vmcnt(8)
	s_waitcnt lgkmcnt(0)
	s_barrier
	s_waitcnt lgkmcnt(7)
	v_mfma_f32_16x16x32_bf16 v[62:65], v[134:137], v[184:187], v[62:65]
	v_mfma_f32_16x16x32_bf16 v[58:61], v[160:163], v[184:187], v[58:61]
	s_waitcnt lgkmcnt(5)
	v_mfma_f32_16x16x32_bf16 v[54:57], v[134:137], v[192:195], v[54:57]
	v_mfma_f32_16x16x32_bf16 v[46:49], v[160:163], v[192:195], v[46:49]
	s_waitcnt lgkmcnt(3)
	v_mfma_f32_16x16x32_bf16 v[38:41], v[134:137], v[200:203], v[38:41]
	v_mfma_f32_16x16x32_bf16 v[30:33], v[160:163], v[200:203], v[30:33]
	s_waitcnt lgkmcnt(1)
	v_mfma_f32_16x16x32_bf16 v[22:25], v[134:137], v[208:211], v[22:25]
	v_mfma_f32_16x16x32_bf16 v[14:17], v[160:163], v[208:211], v[14:17]
	v_mfma_f32_16x16x32_bf16 v[62:65], v[156:159], v[188:191], v[62:65]
	v_mfma_f32_16x16x32_bf16 v[58:61], v[164:167], v[188:191], v[58:61]
	v_mfma_f32_16x16x32_bf16 v[54:57], v[156:159], v[196:199], v[54:57]
	v_mfma_f32_16x16x32_bf16 v[46:49], v[164:167], v[196:199], v[46:49]
	v_mfma_f32_16x16x32_bf16 v[38:41], v[156:159], v[204:207], v[38:41]
	v_mfma_f32_16x16x32_bf16 v[30:33], v[164:167], v[204:207], v[30:33]
	s_waitcnt lgkmcnt(0)
	v_mfma_f32_16x16x32_bf16 v[22:25], v[156:159], v[212:215], v[22:25]
	v_mfma_f32_16x16x32_bf16 v[14:17], v[164:167], v[212:215], v[14:17]
	v_mfma_f32_16x16x32_bf16 v[50:53], v[168:171], v[184:187], v[50:53]
	v_mfma_f32_16x16x32_bf16 v[42:45], v[176:179], v[184:187], v[42:45]
	v_mfma_f32_16x16x32_bf16 v[34:37], v[168:171], v[192:195], v[34:37]
	v_mfma_f32_16x16x32_bf16 v[26:29], v[176:179], v[192:195], v[26:29]
	v_mfma_f32_16x16x32_bf16 v[18:21], v[168:171], v[200:203], v[18:21]
	v_mfma_f32_16x16x32_bf16 v[10:13], v[176:179], v[200:203], v[10:13]
	v_mfma_f32_16x16x32_bf16 v[6:9], v[168:171], v[208:211], v[6:9]
	v_mfma_f32_16x16x32_bf16 v[2:5], v[176:179], v[208:211], v[2:5]
	v_mfma_f32_16x16x32_bf16 v[50:53], v[172:175], v[188:191], v[50:53]
	v_mfma_f32_16x16x32_bf16 v[42:45], v[180:183], v[188:191], v[42:45]
	v_mfma_f32_16x16x32_bf16 v[34:37], v[172:175], v[196:199], v[34:37]
	v_mfma_f32_16x16x32_bf16 v[26:29], v[180:183], v[196:199], v[26:29]
	v_mfma_f32_16x16x32_bf16 v[18:21], v[172:175], v[204:207], v[18:21]
	v_mfma_f32_16x16x32_bf16 v[10:13], v[180:183], v[204:207], v[10:13]
	v_mfma_f32_16x16x32_bf16 v[6:9], v[172:175], v[212:215], v[6:9]
	v_mfma_f32_16x16x32_bf16 v[2:5], v[180:183], v[212:215], v[2:5]
	s_barrier
	ds_read_b128 v[134:137], v153
	ds_read_b128 v[156:159], v153 offset:1024
	ds_read_b128 v[160:163], v153 offset:2048
	ds_read_b128 v[164:167], v153 offset:3072
	ds_read_b128 v[168:171], v154
	ds_read_b128 v[172:175], v154 offset:1024
	ds_read_b128 v[176:179], v154 offset:2048
	ds_read_b128 v[180:183], v154 offset:3072
	s_mov_b32 m0, s36
	s_add_i32 s70, s67, 0x80000
	ds_read_b128 v[184:187], v152 offset:32768
	ds_read_b128 v[188:191], v152 offset:33792
	ds_read_b128 v[192:195], v152 offset:34816
	ds_read_b128 v[196:199], v152 offset:35840
	ds_read_b128 v[200:203], v152 offset:36864
	ds_read_b128 v[204:207], v152 offset:37888
	ds_read_b128 v[208:211], v152 offset:38912
	ds_read_b128 v[212:215], v152 offset:39936
	buffer_load_dwordx4 v131, s[12:15], s70 offen lds
	s_add_i32 s70, s67, 0xc0000
	s_mov_b32 m0, s37
	s_nop 0
	buffer_load_dwordx4 v131, s[12:15], s70 offen lds
	s_waitcnt vmcnt(8)
	s_waitcnt lgkmcnt(0)
	s_barrier
	s_waitcnt lgkmcnt(7)
	v_mfma_f32_16x16x32_bf16 v[126:129], v[134:137], v[184:187], v[126:129]
	v_mfma_f32_16x16x32_bf16 v[122:125], v[160:163], v[184:187], v[122:125]
	s_waitcnt lgkmcnt(5)
	v_mfma_f32_16x16x32_bf16 v[118:121], v[134:137], v[192:195], v[118:121]
	v_mfma_f32_16x16x32_bf16 v[110:113], v[160:163], v[192:195], v[110:113]
	s_waitcnt lgkmcnt(3)
	v_mfma_f32_16x16x32_bf16 v[102:105], v[134:137], v[200:203], v[102:105]
	v_mfma_f32_16x16x32_bf16 v[94:97], v[160:163], v[200:203], v[94:97]
	s_waitcnt lgkmcnt(1)
	v_mfma_f32_16x16x32_bf16 v[86:89], v[134:137], v[208:211], v[86:89]
	v_mfma_f32_16x16x32_bf16 v[78:81], v[160:163], v[208:211], v[78:81]
	v_mfma_f32_16x16x32_bf16 v[126:129], v[156:159], v[188:191], v[126:129]
	v_mfma_f32_16x16x32_bf16 v[122:125], v[164:167], v[188:191], v[122:125]
	v_mfma_f32_16x16x32_bf16 v[118:121], v[156:159], v[196:199], v[118:121]
	v_mfma_f32_16x16x32_bf16 v[110:113], v[164:167], v[196:199], v[110:113]
	v_mfma_f32_16x16x32_bf16 v[102:105], v[156:159], v[204:207], v[102:105]
	v_mfma_f32_16x16x32_bf16 v[94:97], v[164:167], v[204:207], v[94:97]
	s_waitcnt lgkmcnt(0)
	v_mfma_f32_16x16x32_bf16 v[86:89], v[156:159], v[212:215], v[86:89]
	v_mfma_f32_16x16x32_bf16 v[78:81], v[164:167], v[212:215], v[78:81]
	v_mfma_f32_16x16x32_bf16 v[114:117], v[168:171], v[184:187], v[114:117]
	v_mfma_f32_16x16x32_bf16 v[106:109], v[176:179], v[184:187], v[106:109]
	v_mfma_f32_16x16x32_bf16 v[98:101], v[168:171], v[192:195], v[98:101]
	v_mfma_f32_16x16x32_bf16 v[90:93], v[176:179], v[192:195], v[90:93]
	v_mfma_f32_16x16x32_bf16 v[82:85], v[168:171], v[200:203], v[82:85]
	v_mfma_f32_16x16x32_bf16 v[74:77], v[176:179], v[200:203], v[74:77]
	v_mfma_f32_16x16x32_bf16 v[70:73], v[168:171], v[208:211], v[70:73]
	v_mfma_f32_16x16x32_bf16 v[66:69], v[176:179], v[208:211], v[66:69]
	v_mfma_f32_16x16x32_bf16 v[114:117], v[172:175], v[188:191], v[114:117]
	v_mfma_f32_16x16x32_bf16 v[106:109], v[180:183], v[188:191], v[106:109]
	v_mfma_f32_16x16x32_bf16 v[98:101], v[172:175], v[196:199], v[98:101]
	v_mfma_f32_16x16x32_bf16 v[90:93], v[180:183], v[196:199], v[90:93]
	v_mfma_f32_16x16x32_bf16 v[82:85], v[172:175], v[204:207], v[82:85]
	v_mfma_f32_16x16x32_bf16 v[74:77], v[180:183], v[204:207], v[74:77]
	v_mfma_f32_16x16x32_bf16 v[70:73], v[172:175], v[212:215], v[70:73]
	v_mfma_f32_16x16x32_bf16 v[66:69], v[180:183], v[212:215], v[66:69]
	s_barrier
	s_mov_b32 m0, s39
	s_add_i32 s70, s69, 0x80
	ds_read_b128 v[184:187], v152 offset:49152
	ds_read_b128 v[188:191], v152 offset:50176
	ds_read_b128 v[192:195], v152 offset:51200
	ds_read_b128 v[196:199], v152 offset:52224
	ds_read_b128 v[200:203], v152 offset:53248
	ds_read_b128 v[204:207], v152 offset:54272
	ds_read_b128 v[208:211], v152 offset:55296
	ds_read_b128 v[212:215], v152 offset:56320
	buffer_load_dwordx4 v148, s[12:15], s70 offen lds
	s_add_i32 s70, s69, 0x40080
	s_mov_b32 m0, s40
	s_add_i32 s67, s67, 0x40080
	buffer_load_dwordx4 v148, s[12:15], s70 offen lds
	s_add_i32 s70, s69, 0x80080
	s_mov_b32 m0, s43
	s_add_i32 s69, s69, 0xc0080
	buffer_load_dwordx4 v148, s[12:15], s70 offen lds
	s_mov_b32 m0, s49
	s_nop 0
	buffer_load_dwordx4 v148, s[12:15], s69 offen lds
	s_mov_b32 m0, s41
	s_nop 0
	buffer_load_dwordx4 v131, s[12:15], s68 offen lds
	s_mov_b32 m0, s42
	s_nop 0
	buffer_load_dwordx4 v131, s[12:15], s67 offen lds
	s_waitcnt vmcnt(8)
	s_waitcnt lgkmcnt(0)
	s_barrier
	s_waitcnt lgkmcnt(7)
	v_mfma_f32_16x16x32_bf16 v[62:65], v[134:137], v[184:187], v[62:65]
	v_mfma_f32_16x16x32_bf16 v[58:61], v[160:163], v[184:187], v[58:61]
	s_waitcnt lgkmcnt(5)
	v_mfma_f32_16x16x32_bf16 v[54:57], v[134:137], v[192:195], v[54:57]
	v_mfma_f32_16x16x32_bf16 v[46:49], v[160:163], v[192:195], v[46:49]
	s_waitcnt lgkmcnt(3)
	v_mfma_f32_16x16x32_bf16 v[38:41], v[134:137], v[200:203], v[38:41]
	v_mfma_f32_16x16x32_bf16 v[30:33], v[160:163], v[200:203], v[30:33]
	s_waitcnt lgkmcnt(1)
	v_mfma_f32_16x16x32_bf16 v[22:25], v[134:137], v[208:211], v[22:25]
	v_mfma_f32_16x16x32_bf16 v[14:17], v[160:163], v[208:211], v[14:17]
	v_mfma_f32_16x16x32_bf16 v[62:65], v[156:159], v[188:191], v[62:65]
	v_mfma_f32_16x16x32_bf16 v[58:61], v[164:167], v[188:191], v[58:61]
	v_mfma_f32_16x16x32_bf16 v[54:57], v[156:159], v[196:199], v[54:57]
	v_mfma_f32_16x16x32_bf16 v[46:49], v[164:167], v[196:199], v[46:49]
	v_mfma_f32_16x16x32_bf16 v[38:41], v[156:159], v[204:207], v[38:41]
	v_mfma_f32_16x16x32_bf16 v[30:33], v[164:167], v[204:207], v[30:33]
	s_waitcnt lgkmcnt(0)
	v_mfma_f32_16x16x32_bf16 v[22:25], v[156:159], v[212:215], v[22:25]
	v_mfma_f32_16x16x32_bf16 v[14:17], v[164:167], v[212:215], v[14:17]
	v_mfma_f32_16x16x32_bf16 v[50:53], v[168:171], v[184:187], v[50:53]
	v_mfma_f32_16x16x32_bf16 v[42:45], v[176:179], v[184:187], v[42:45]
	v_mfma_f32_16x16x32_bf16 v[34:37], v[168:171], v[192:195], v[34:37]
	v_mfma_f32_16x16x32_bf16 v[26:29], v[176:179], v[192:195], v[26:29]
	v_mfma_f32_16x16x32_bf16 v[18:21], v[168:171], v[200:203], v[18:21]
	v_mfma_f32_16x16x32_bf16 v[10:13], v[176:179], v[200:203], v[10:13]
	v_mfma_f32_16x16x32_bf16 v[6:9], v[168:171], v[208:211], v[6:9]
	v_mfma_f32_16x16x32_bf16 v[2:5], v[176:179], v[208:211], v[2:5]
	v_mfma_f32_16x16x32_bf16 v[50:53], v[172:175], v[188:191], v[50:53]
	v_mfma_f32_16x16x32_bf16 v[42:45], v[180:183], v[188:191], v[42:45]
	v_mfma_f32_16x16x32_bf16 v[34:37], v[172:175], v[196:199], v[34:37]
	v_mfma_f32_16x16x32_bf16 v[26:29], v[180:183], v[196:199], v[26:29]
	v_mfma_f32_16x16x32_bf16 v[18:21], v[172:175], v[204:207], v[18:21]
	v_mfma_f32_16x16x32_bf16 v[10:13], v[180:183], v[204:207], v[10:13]
	v_mfma_f32_16x16x32_bf16 v[6:9], v[172:175], v[212:215], v[6:9]
	v_mfma_f32_16x16x32_bf16 v[2:5], v[180:183], v[212:215], v[2:5]
	s_barrier
	s_add_i32 s65, s65, 2
	s_addk_i32 s8, 0x100
	s_addk_i32 s9, 0x100
	s_cmp_gt_u32 s65, 29
	s_cbranch_scc0 .LBB0_191
	s_and_b64 vcc, exec, s[22:23]
	s_cbranch_vccz .LBB0_194
	s_barrier

.LBB0_261:
	ds_read_b128 v[132:135], v144
	ds_read_b128 v[136:139], v144 offset:1024
	ds_read_b128 v[152:155], v144 offset:2048
	ds_read_b128 v[156:159], v144 offset:3072
	ds_read_b128 v[160:163], v145
	ds_read_b128 v[164:167], v145 offset:1024
	ds_read_b128 v[168:171], v145 offset:2048
	ds_read_b128 v[172:175], v145 offset:3072
	s_add_i32 s12, s34, 0xfffa0080
	s_cmp_eq_u32 s75, 12
	s_cselect_b32 s76, s72, s12
	s_cselect_b32 s78, s73, s35
	s_add_i32 s77, s76, 0x80
	s_add_i32 s79, s34, 0xfffe0000
	s_mov_b32 s12, s44
	s_mov_b32 m0, s58
	ds_read_b128 v[176:179], v146
	ds_read_b128 v[180:183], v146 offset:1024
	ds_read_b128 v[184:187], v146 offset:2048
	ds_read_b128 v[188:191], v146 offset:3072
	ds_read_b128 v[192:195], v146 offset:4096
	ds_read_b128 v[196:199], v146 offset:5120
	ds_read_b128 v[200:203], v146 offset:6144
	ds_read_b128 v[204:207], v146 offset:7168
	buffer_load_dwordx4 v142, s[12:15], s79 offen lds
	s_mov_b32 m0, s59
	s_nop 0
	buffer_load_dwordx4 v142, s[12:15], s34 offen lds
	s_waitcnt vmcnt(8)
	s_waitcnt lgkmcnt(0)
	s_barrier
	s_waitcnt lgkmcnt(6)
	v_mfma_scale_f32_16x16x128_f8f6f4 v[126:129], v[132:139], v[176:183], v[126:129], v148, v147 op_sel_hi:[0,0,0]
	v_mfma_scale_f32_16x16x128_f8f6f4 v[122:125], v[152:159], v[176:183], v[122:125], v148, v147 op_sel_hi:[0,0,0]
	s_waitcnt lgkmcnt(4)
	v_mfma_scale_f32_16x16x128_f8f6f4 v[118:121], v[132:139], v[184:191], v[118:121], v148, v147 op_sel_hi:[0,0,0]
	v_mfma_scale_f32_16x16x128_f8f6f4 v[114:117], v[152:159], v[184:191], v[114:117], v148, v147 op_sel_hi:[0,0,0]
	s_waitcnt lgkmcnt(2)
	v_mfma_scale_f32_16x16x128_f8f6f4 v[102:105], v[132:139], v[192:199], v[102:105], v148, v147 op_sel_hi:[0,0,0]
	v_mfma_scale_f32_16x16x128_f8f6f4 v[98:101], v[152:159], v[192:199], v[98:101], v148, v147 op_sel_hi:[0,0,0]
	s_waitcnt lgkmcnt(0)
	v_mfma_scale_f32_16x16x128_f8f6f4 v[208:211], v[132:139], v[200:207], v[86:89], v148, v147 op_sel_hi:[0,0,0]
	v_mfma_scale_f32_16x16x128_f8f6f4 v[212:215], v[152:159], v[200:207], v[82:85], v148, v147 op_sel_hi:[0,0,0]
	v_mfma_scale_f32_16x16x128_f8f6f4 v[110:113], v[160:167], v[176:183], v[110:113], v148, v147 op_sel_hi:[0,0,0]
	v_mfma_scale_f32_16x16x128_f8f6f4 v[106:109], v[168:175], v[176:183], v[106:109], v148, v147 op_sel_hi:[0,0,0]
	v_mfma_scale_f32_16x16x128_f8f6f4 v[176:179], v[160:167], v[184:191], v[94:97], v148, v147 op_sel_hi:[0,0,0]
	v_mfma_scale_f32_16x16x128_f8f6f4 v[180:183], v[168:175], v[184:191], v[90:93], v148, v147 op_sel_hi:[0,0,0]
	v_mfma_scale_f32_16x16x128_f8f6f4 v[184:187], v[160:167], v[192:199], v[78:81], v148, v147 op_sel_hi:[0,0,0]
	v_mfma_scale_f32_16x16x128_f8f6f4 v[188:191], v[168:175], v[192:199], v[74:77], v148, v147 op_sel_hi:[0,0,0]
	v_mfma_scale_f32_16x16x128_f8f6f4 v[192:195], v[160:167], v[200:207], v[70:73], v148, v147 op_sel_hi:[0,0,0]
	v_mfma_scale_f32_16x16x128_f8f6f4 v[196:199], v[168:175], v[200:207], v[66:69], v148, v147 op_sel_hi:[0,0,0]
	s_barrier
	s_mov_b32 m0, s23
	s_nop 3
	ds_read_b128 v[66:69], v146 offset:16384
	ds_read_b128 v[70:73], v146 offset:17408
	ds_read_b128 v[74:77], v146 offset:18432
	ds_read_b128 v[78:81], v146 offset:19456
	ds_read_b128 v[82:85], v146 offset:20480
	ds_read_b128 v[86:89], v146 offset:21504
	ds_read_b128 v[90:93], v146 offset:22528
	ds_read_b128 v[94:97], v146 offset:23552
	buffer_load_dwordx4 v143, s[12:15], s78 offen lds
	s_add_i32 s79, s78, 0x20000
	s_mov_b32 m0, s36
	s_nop 0
	buffer_load_dwordx4 v143, s[12:15], s79 offen lds
	s_add_i32 s79, s78, 0x40000
	s_mov_b32 m0, s37
	s_nop 0
	buffer_load_dwordx4 v143, s[12:15], s79 offen lds
	s_add_i32 s79, s78, 0x60000
	s_mov_b32 m0, s38
	s_nop 0
	buffer_load_dwordx4 v143, s[12:15], s79 offen lds
	s_mov_b32 m0, s3
	s_add_i32 s79, s76, 0x20000
	buffer_load_dwordx4 v142, s[12:15], s76 offen lds
	s_mov_b32 m0, s39
	s_nop 0
	buffer_load_dwordx4 v142, s[12:15], s79 offen lds
	s_waitcnt vmcnt(8)
	s_waitcnt lgkmcnt(0)
	s_barrier
	s_waitcnt lgkmcnt(6)
	v_mfma_scale_f32_16x16x128_f8f6f4 v[62:65], v[132:139], v[66:73], v[62:65], v148, v147 op_sel_hi:[0,0,0]
	v_mfma_scale_f32_16x16x128_f8f6f4 v[58:61], v[152:159], v[66:73], v[58:61], v148, v147 op_sel_hi:[0,0,0]
	s_waitcnt lgkmcnt(4)
	v_mfma_scale_f32_16x16x128_f8f6f4 v[54:57], v[132:139], v[74:81], v[54:57], v148, v147 op_sel_hi:[0,0,0]
	v_mfma_scale_f32_16x16x128_f8f6f4 v[50:53], v[152:159], v[74:81], v[50:53], v148, v147 op_sel_hi:[0,0,0]
	s_waitcnt lgkmcnt(2)
	v_mfma_scale_f32_16x16x128_f8f6f4 v[200:203], v[132:139], v[82:89], v[38:41], v148, v147 op_sel_hi:[0,0,0]
	v_mfma_scale_f32_16x16x128_f8f6f4 v[204:207], v[152:159], v[82:89], v[34:37], v148, v147 op_sel_hi:[0,0,0]
	s_waitcnt lgkmcnt(0)
	v_mfma_scale_f32_16x16x128_f8f6f4 v[216:219], v[132:139], v[90:97], v[22:25], v148, v147 op_sel_hi:[0,0,0]
	v_mfma_scale_f32_16x16x128_f8f6f4 v[220:223], v[152:159], v[90:97], v[18:21], v148, v147 op_sel_hi:[0,0,0]
	v_mfma_scale_f32_16x16x128_f8f6f4 v[224:227], v[160:167], v[66:73], v[46:49], v148, v147 op_sel_hi:[0,0,0]
	v_mfma_scale_f32_16x16x128_f8f6f4 v[228:231], v[168:175], v[66:73], v[42:45], v148, v147 op_sel_hi:[0,0,0]
	v_mfma_scale_f32_16x16x128_f8f6f4 v[232:235], v[160:167], v[74:81], v[30:33], v148, v147 op_sel_hi:[0,0,0]
	v_mfma_scale_f32_16x16x128_f8f6f4 v[236:239], v[168:175], v[74:81], v[26:29], v148, v147 op_sel_hi:[0,0,0]
	v_mfma_scale_f32_16x16x128_f8f6f4 v[240:243], v[160:167], v[82:89], v[14:17], v148, v147 op_sel_hi:[0,0,0]
	v_mfma_scale_f32_16x16x128_f8f6f4 v[244:247], v[168:175], v[82:89], v[10:13], v148, v147 op_sel_hi:[0,0,0]
	v_mfma_scale_f32_16x16x128_f8f6f4 v[248:251], v[160:167], v[90:97], v[6:9], v148, v147 op_sel_hi:[0,0,0]
	v_mfma_scale_f32_16x16x128_f8f6f4 v[252:255], v[168:175], v[90:97], v[2:5], v148, v147 op_sel_hi:[0,0,0]
	s_barrier
	s_nop 4
	ds_read_b128 v[2:5], v149
	ds_read_b128 v[6:9], v149 offset:1024
	ds_read_b128 v[10:13], v149 offset:2048
	ds_read_b128 v[14:17], v149 offset:3072
	ds_read_b128 v[132:135], v150
	ds_read_b128 v[136:139], v150 offset:1024
	ds_read_b128 v[152:155], v150 offset:2048
	ds_read_b128 v[156:159], v150 offset:3072
	s_mov_b32 m0, s40
	s_add_i32 s79, s76, 0x40000
	ds_read_b128 v[18:21], v146 offset:32768
	ds_read_b128 v[22:25], v146 offset:33792
	ds_read_b128 v[26:29], v146 offset:34816
	ds_read_b128 v[30:33], v146 offset:35840
	ds_read_b128 v[34:37], v146 offset:36864
	ds_read_b128 v[38:41], v146 offset:37888
	ds_read_b128 v[42:45], v146 offset:38912
	ds_read_b128 v[46:49], v146 offset:39936
	buffer_load_dwordx4 v142, s[12:15], s79 offen lds
	s_add_i32 s79, s76, 0x60000
	s_mov_b32 m0, s41
	s_nop 0
	buffer_load_dwordx4 v142, s[12:15], s79 offen lds
	s_waitcnt vmcnt(8)
	s_waitcnt lgkmcnt(0)
	s_barrier
	s_waitcnt lgkmcnt(6)
	v_mfma_scale_f32_16x16x128_f8f6f4 v[126:129], v[2:9], v[18:25], v[126:129], v148, v147 op_sel_hi:[0,0,0]
	v_mfma_scale_f32_16x16x128_f8f6f4 v[122:125], v[10:17], v[18:25], v[122:125], v148, v147 op_sel_hi:[0,0,0]
	s_waitcnt lgkmcnt(4)
	v_mfma_scale_f32_16x16x128_f8f6f4 v[118:121], v[2:9], v[26:33], v[118:121], v148, v147 op_sel_hi:[0,0,0]
	v_mfma_scale_f32_16x16x128_f8f6f4 v[114:117], v[10:17], v[26:33], v[114:117], v148, v147 op_sel_hi:[0,0,0]
	s_waitcnt lgkmcnt(2)
	v_mfma_scale_f32_16x16x128_f8f6f4 v[102:105], v[2:9], v[34:41], v[102:105], v148, v147 op_sel_hi:[0,0,0]
	v_mfma_scale_f32_16x16x128_f8f6f4 v[98:101], v[10:17], v[34:41], v[98:101], v148, v147 op_sel_hi:[0,0,0]
	s_waitcnt lgkmcnt(0)
	v_mfma_scale_f32_16x16x128_f8f6f4 v[86:89], v[2:9], v[42:49], v[208:211], v148, v147 op_sel_hi:[0,0,0]
	v_mfma_scale_f32_16x16x128_f8f6f4 v[82:85], v[10:17], v[42:49], v[212:215], v148, v147 op_sel_hi:[0,0,0]
	v_mfma_scale_f32_16x16x128_f8f6f4 v[110:113], v[132:139], v[18:25], v[110:113], v148, v147 op_sel_hi:[0,0,0]
	v_mfma_scale_f32_16x16x128_f8f6f4 v[106:109], v[152:159], v[18:25], v[106:109], v148, v147 op_sel_hi:[0,0,0]
	v_mfma_scale_f32_16x16x128_f8f6f4 v[94:97], v[132:139], v[26:33], v[176:179], v148, v147 op_sel_hi:[0,0,0]
	v_mfma_scale_f32_16x16x128_f8f6f4 v[90:93], v[152:159], v[26:33], v[180:183], v148, v147 op_sel_hi:[0,0,0]
	v_mfma_scale_f32_16x16x128_f8f6f4 v[78:81], v[132:139], v[34:41], v[184:187], v148, v147 op_sel_hi:[0,0,0]
	v_mfma_scale_f32_16x16x128_f8f6f4 v[74:77], v[152:159], v[34:41], v[188:191], v148, v147 op_sel_hi:[0,0,0]
	v_mfma_scale_f32_16x16x128_f8f6f4 v[70:73], v[132:139], v[42:49], v[192:195], v148, v147 op_sel_hi:[0,0,0]
	v_mfma_scale_f32_16x16x128_f8f6f4 v[66:69], v[152:159], v[42:49], v[196:199], v148, v147 op_sel_hi:[0,0,0]
	s_barrier
	s_mov_b32 m0, s49
	s_add_i32 s79, s78, 0x80
	ds_read_b128 v[26:29], v146 offset:49152
	ds_read_b128 v[30:33], v146 offset:50176
	ds_read_b128 v[160:163], v146 offset:51200
	ds_read_b128 v[164:167], v146 offset:52224
	ds_read_b128 v[168:171], v146 offset:53248
	ds_read_b128 v[172:175], v146 offset:54272
	ds_read_b128 v[176:179], v146 offset:55296
	ds_read_b128 v[180:183], v146 offset:56320
	buffer_load_dwordx4 v143, s[12:15], s79 offen lds
	s_add_i32 s79, s78, 0x20080
	s_mov_b32 m0, s53
	s_add_i32 s76, s76, 0x20080
	buffer_load_dwordx4 v143, s[12:15], s79 offen lds
	s_add_i32 s79, s78, 0x40080
	s_mov_b32 m0, s56
	s_add_i32 s78, s78, 0x60080
	buffer_load_dwordx4 v143, s[12:15], s79 offen lds
	s_mov_b32 m0, s57
	s_nop 0
	buffer_load_dwordx4 v143, s[12:15], s78 offen lds
	s_mov_b32 m0, s54
	s_nop 0
	buffer_load_dwordx4 v142, s[12:15], s77 offen lds
	s_mov_b32 m0, s55
	s_nop 0
	buffer_load_dwordx4 v142, s[12:15], s76 offen lds
	s_waitcnt vmcnt(8)
	s_waitcnt lgkmcnt(0)
	s_barrier
	s_waitcnt lgkmcnt(6)
	v_mfma_scale_f32_16x16x128_f8f6f4 v[62:65], v[2:9], v[26:33], v[62:65], v148, v147 op_sel_hi:[0,0,0]
	v_mfma_scale_f32_16x16x128_f8f6f4 v[58:61], v[10:17], v[26:33], v[58:61], v148, v147 op_sel_hi:[0,0,0]
	s_waitcnt lgkmcnt(4)
	v_mfma_scale_f32_16x16x128_f8f6f4 v[54:57], v[2:9], v[160:167], v[54:57], v148, v147 op_sel_hi:[0,0,0]
	v_mfma_scale_f32_16x16x128_f8f6f4 v[50:53], v[10:17], v[160:167], v[50:53], v148, v147 op_sel_hi:[0,0,0]
	s_waitcnt lgkmcnt(2)
	v_mfma_scale_f32_16x16x128_f8f6f4 v[38:41], v[2:9], v[168:175], v[200:203], v148, v147 op_sel_hi:[0,0,0]
	v_mfma_scale_f32_16x16x128_f8f6f4 v[34:37], v[10:17], v[168:175], v[204:207], v148, v147 op_sel_hi:[0,0,0]
	s_waitcnt lgkmcnt(0)
	v_mfma_scale_f32_16x16x128_f8f6f4 v[22:25], v[2:9], v[176:183], v[216:219], v148, v147 op_sel_hi:[0,0,0]
	v_mfma_scale_f32_16x16x128_f8f6f4 v[18:21], v[10:17], v[176:183], v[220:223], v148, v147 op_sel_hi:[0,0,0]
	v_mfma_scale_f32_16x16x128_f8f6f4 v[46:49], v[132:139], v[26:33], v[224:227], v148, v147 op_sel_hi:[0,0,0]
	v_mfma_scale_f32_16x16x128_f8f6f4 v[42:45], v[152:159], v[26:33], v[228:231], v148, v147 op_sel_hi:[0,0,0]
	v_mfma_scale_f32_16x16x128_f8f6f4 v[30:33], v[132:139], v[160:167], v[232:235], v148, v147 op_sel_hi:[0,0,0]
	v_mfma_scale_f32_16x16x128_f8f6f4 v[26:29], v[152:159], v[160:167], v[236:239], v148, v147 op_sel_hi:[0,0,0]
	v_mfma_scale_f32_16x16x128_f8f6f4 v[14:17], v[132:139], v[168:175], v[240:243], v148, v147 op_sel_hi:[0,0,0]
	v_mfma_scale_f32_16x16x128_f8f6f4 v[10:13], v[152:159], v[168:175], v[244:247], v148, v147 op_sel_hi:[0,0,0]
	v_mfma_scale_f32_16x16x128_f8f6f4 v[6:9], v[132:139], v[176:183], v[248:251], v148, v147 op_sel_hi:[0,0,0]
	v_mfma_scale_f32_16x16x128_f8f6f4 v[2:5], v[152:159], v[176:183], v[252:255], v148, v147 op_sel_hi:[0,0,0]
	s_barrier
	s_add_i32 s75, s75, 2
	s_addk_i32 s34, 0x100
	s_addk_i32 s35, 0x100
	s_cmp_gt_u32 s75, 13
	s_cbranch_scc0 .LBB0_261
	s_and_b64 vcc, exec, s[20:21]
	s_cbranch_vccz .LBB0_264
	s_barrier

.LBB0_1820:
	v_add_u32_e32 v11, 0x10000, v231
	ds_read_b128 v[2:5], v11
	ds_read_b128 v[6:9], v11 offset:1024
	ds_read_b128 v[150:153], v11 offset:2048
	ds_read_b128 v[154:157], v11 offset:3072
	v_add_u32_e32 v11, 0x14000, v231
	ds_read_b128 v[158:161], v11
	ds_read_b128 v[162:165], v11 offset:1024
	ds_read_b128 v[166:169], v11 offset:2048
	ds_read_b128 v[170:173], v11 offset:3072
	s_add_i32 s8, s6, 0xfffd0080
	s_cmp_eq_u32 s24, 4
	s_cselect_b32 s25, s63, s8
	s_cselect_b32 s68, s64, s7
	s_add_i32 s67, s25, 0x80
	s_add_i32 s69, s6, 0xffff0000
	s_mov_b32 s8, s44
	s_mov_b32 m0, s43
	ds_read_b128 v[174:177], v232
	ds_read_b128 v[178:181], v232 offset:1024
	ds_read_b128 v[182:185], v232 offset:2048
	ds_read_b128 v[186:189], v232 offset:3072
	ds_read_b128 v[190:193], v232 offset:4096
	ds_read_b128 v[194:197], v232 offset:5120
	ds_read_b128 v[198:201], v232 offset:6144
	ds_read_b128 v[202:205], v232 offset:7168
	buffer_load_dwordx4 v1, s[8:11], s69 offen lds
	s_mov_b32 m0, s49
	s_nop 0
	buffer_load_dwordx4 v1, s[8:11], s6 offen lds
	s_waitcnt vmcnt(8)
	s_waitcnt lgkmcnt(0)
	s_barrier
	s_waitcnt lgkmcnt(6)
	v_mfma_scale_f32_16x16x128_f8f6f4 v[138:141], v[2:9], v[174:181], v[138:141], v233, v233 op_sel_hi:[0,0,0]
	v_mfma_scale_f32_16x16x128_f8f6f4 v[134:137], v[150:157], v[174:181], v[134:137], v233, v233 op_sel_hi:[0,0,0]
	s_waitcnt lgkmcnt(4)
	v_mfma_scale_f32_16x16x128_f8f6f4 v[130:133], v[2:9], v[182:189], v[130:133], v233, v233 op_sel_hi:[0,0,0]
	v_mfma_scale_f32_16x16x128_f8f6f4 v[126:129], v[150:157], v[182:189], v[126:129], v233, v233 op_sel_hi:[0,0,0]
	s_waitcnt lgkmcnt(2)
	v_mfma_scale_f32_16x16x128_f8f6f4 v[122:125], v[2:9], v[190:197], v[122:125], v233, v233 op_sel_hi:[0,0,0]
	v_mfma_scale_f32_16x16x128_f8f6f4 v[118:121], v[150:157], v[190:197], v[118:121], v233, v233 op_sel_hi:[0,0,0]
	s_waitcnt lgkmcnt(0)
	v_mfma_scale_f32_16x16x128_f8f6f4 v[114:117], v[2:9], v[198:205], v[114:117], v233, v233 op_sel_hi:[0,0,0]
	v_mfma_scale_f32_16x16x128_f8f6f4 v[110:113], v[150:157], v[198:205], v[110:113], v233, v233 op_sel_hi:[0,0,0]
	v_mfma_scale_f32_16x16x128_f8f6f4 v[142:145], v[158:165], v[174:181], v[106:109], v233, v233 op_sel_hi:[0,0,0]
	v_mfma_scale_f32_16x16x128_f8f6f4 v[174:177], v[166:173], v[174:181], v[102:105], v233, v233 op_sel_hi:[0,0,0]
	v_mfma_scale_f32_16x16x128_f8f6f4 v[178:181], v[158:165], v[182:189], v[98:101], v233, v233 op_sel_hi:[0,0,0]
	v_mfma_scale_f32_16x16x128_f8f6f4 v[182:185], v[166:173], v[182:189], v[94:97], v233, v233 op_sel_hi:[0,0,0]
	v_mfma_scale_f32_16x16x128_f8f6f4 v[186:189], v[158:165], v[190:197], v[90:93], v233, v233 op_sel_hi:[0,0,0]
	v_mfma_scale_f32_16x16x128_f8f6f4 v[190:193], v[166:173], v[190:197], v[86:89], v233, v233 op_sel_hi:[0,0,0]
	v_mfma_scale_f32_16x16x128_f8f6f4 v[194:197], v[158:165], v[198:205], v[82:85], v233, v233 op_sel_hi:[0,0,0]
	v_mfma_scale_f32_16x16x128_f8f6f4 v[198:201], v[166:173], v[198:205], v[78:81], v233, v233 op_sel_hi:[0,0,0]
	s_barrier
	s_mov_b32 m0, s26
	s_nop 3
	ds_read_b128 v[78:81], v232 offset:16384
	ds_read_b128 v[82:85], v232 offset:17408
	ds_read_b128 v[86:89], v232 offset:18432
	ds_read_b128 v[90:93], v232 offset:19456
	ds_read_b128 v[94:97], v232 offset:20480
	ds_read_b128 v[98:101], v232 offset:21504
	ds_read_b128 v[102:105], v232 offset:22528
	ds_read_b128 v[106:109], v232 offset:23552
	buffer_load_dwordx4 v230, s[8:11], s68 offen lds
	s_add_i32 s69, s68, 0x10000
	s_mov_b32 m0, s27
	s_nop 0
	buffer_load_dwordx4 v230, s[8:11], s69 offen lds
	s_add_i32 s69, s68, 0x20000
	s_mov_b32 m0, s28
	s_nop 0
	buffer_load_dwordx4 v230, s[8:11], s69 offen lds
	s_add_i32 s69, s68, 0x30000
	s_mov_b32 m0, s29
	s_nop 0
	buffer_load_dwordx4 v230, s[8:11], s69 offen lds
	s_mov_b32 m0, s3
	s_add_i32 s69, s25, 0x10000
	buffer_load_dwordx4 v1, s[8:11], s25 offen lds
	s_mov_b32 m0, s30
	s_nop 0
	buffer_load_dwordx4 v1, s[8:11], s69 offen lds
	s_waitcnt vmcnt(8)
	s_waitcnt lgkmcnt(0)
	s_barrier
	s_waitcnt lgkmcnt(6)
	v_mfma_scale_f32_16x16x128_f8f6f4 v[74:77], v[2:9], v[78:85], v[74:77], v233, v233 op_sel_hi:[0,0,0]
	v_mfma_scale_f32_16x16x128_f8f6f4 v[70:73], v[150:157], v[78:85], v[70:73], v233, v233 op_sel_hi:[0,0,0]
	s_waitcnt lgkmcnt(4)
	v_mfma_scale_f32_16x16x128_f8f6f4 v[66:69], v[2:9], v[86:93], v[66:69], v233, v233 op_sel_hi:[0,0,0]
	v_mfma_scale_f32_16x16x128_f8f6f4 v[62:65], v[150:157], v[86:93], v[62:65], v233, v233 op_sel_hi:[0,0,0]
	s_waitcnt lgkmcnt(2)
	v_mfma_scale_f32_16x16x128_f8f6f4 v[58:61], v[2:9], v[94:101], v[58:61], v233, v233 op_sel_hi:[0,0,0]
	v_mfma_scale_f32_16x16x128_f8f6f4 v[54:57], v[150:157], v[94:101], v[54:57], v233, v233 op_sel_hi:[0,0,0]
	s_waitcnt lgkmcnt(0)
	v_mfma_scale_f32_16x16x128_f8f6f4 v[202:205], v[2:9], v[102:109], v[50:53], v233, v233 op_sel_hi:[0,0,0]
	v_mfma_scale_f32_16x16x128_f8f6f4 v[206:209], v[150:157], v[102:109], v[46:49], v233, v233 op_sel_hi:[0,0,0]
	v_mfma_scale_f32_16x16x128_f8f6f4 v[210:213], v[158:165], v[78:85], v[42:45], v233, v233 op_sel_hi:[0,0,0]
	v_mfma_scale_f32_16x16x128_f8f6f4 v[214:217], v[166:173], v[78:85], v[38:41], v233, v233 op_sel_hi:[0,0,0]
	v_mfma_scale_f32_16x16x128_f8f6f4 v[218:221], v[158:165], v[86:93], v[34:37], v233, v233 op_sel_hi:[0,0,0]
	v_mfma_scale_f32_16x16x128_f8f6f4 v[222:225], v[166:173], v[86:93], v[30:33], v233, v233 op_sel_hi:[0,0,0]
	v_mfma_scale_f32_16x16x128_f8f6f4 v[226:229], v[158:165], v[94:101], v[26:29], v233, v233 op_sel_hi:[0,0,0]
	v_mfma_scale_f32_16x16x128_f8f6f4 v[236:239], v[166:173], v[94:101], v[22:25], v233, v233 op_sel_hi:[0,0,0]
	v_mfma_scale_f32_16x16x128_f8f6f4 v[240:243], v[158:165], v[102:109], v[18:21], v233, v233 op_sel_hi:[0,0,0]
	v_mfma_scale_f32_16x16x128_f8f6f4 v[244:247], v[166:173], v[102:109], v[14:17], v233, v233 op_sel_hi:[0,0,0]
	s_barrier
	v_add_u32_e32 v11, 0x18000, v231
	ds_read_b128 v[2:5], v11
	ds_read_b128 v[6:9], v11 offset:1024
	s_nop 1
	ds_read_b128 v[12:15], v11 offset:2048
	ds_read_b128 v[16:19], v11 offset:3072
	v_add_u32_e32 v11, 0x1c000, v231
	ds_read_b128 v[150:153], v11
	ds_read_b128 v[154:157], v11 offset:1024
	ds_read_b128 v[158:161], v11 offset:2048
	ds_read_b128 v[162:165], v11 offset:3072
	s_mov_b32 m0, s31
	s_add_i32 s69, s25, 0x20000
	ds_read_b128 v[20:23], v232 offset:32768
	ds_read_b128 v[24:27], v232 offset:33792
	ds_read_b128 v[28:31], v232 offset:34816
	ds_read_b128 v[32:35], v232 offset:35840
	ds_read_b128 v[36:39], v232 offset:36864
	ds_read_b128 v[40:43], v232 offset:37888
	ds_read_b128 v[44:47], v232 offset:38912
	ds_read_b128 v[48:51], v232 offset:39936
	buffer_load_dwordx4 v1, s[8:11], s69 offen lds
	s_add_i32 s69, s25, 0x30000
	s_mov_b32 m0, s34
	s_nop 0
	buffer_load_dwordx4 v1, s[8:11], s69 offen lds
	s_waitcnt vmcnt(8)
	s_waitcnt lgkmcnt(0)
	s_barrier
	s_waitcnt lgkmcnt(6)
	v_mfma_scale_f32_16x16x128_f8f6f4 v[138:141], v[2:9], v[20:27], v[138:141], v233, v233 op_sel_hi:[0,0,0]
	v_mfma_scale_f32_16x16x128_f8f6f4 v[134:137], v[12:19], v[20:27], v[134:137], v233, v233 op_sel_hi:[0,0,0]
	s_waitcnt lgkmcnt(4)
	v_mfma_scale_f32_16x16x128_f8f6f4 v[130:133], v[2:9], v[28:35], v[130:133], v233, v233 op_sel_hi:[0,0,0]
	v_mfma_scale_f32_16x16x128_f8f6f4 v[126:129], v[12:19], v[28:35], v[126:129], v233, v233 op_sel_hi:[0,0,0]
	s_waitcnt lgkmcnt(2)
	v_mfma_scale_f32_16x16x128_f8f6f4 v[122:125], v[2:9], v[36:43], v[122:125], v233, v233 op_sel_hi:[0,0,0]
	v_mfma_scale_f32_16x16x128_f8f6f4 v[118:121], v[12:19], v[36:43], v[118:121], v233, v233 op_sel_hi:[0,0,0]
	s_waitcnt lgkmcnt(0)
	v_mfma_scale_f32_16x16x128_f8f6f4 v[114:117], v[2:9], v[44:51], v[114:117], v233, v233 op_sel_hi:[0,0,0]
	v_mfma_scale_f32_16x16x128_f8f6f4 v[110:113], v[12:19], v[44:51], v[110:113], v233, v233 op_sel_hi:[0,0,0]
	v_mfma_scale_f32_16x16x128_f8f6f4 v[106:109], v[150:157], v[20:27], v[142:145], v233, v233 op_sel_hi:[0,0,0]
	v_mfma_scale_f32_16x16x128_f8f6f4 v[102:105], v[158:165], v[20:27], v[174:177], v233, v233 op_sel_hi:[0,0,0]
	v_mfma_scale_f32_16x16x128_f8f6f4 v[98:101], v[150:157], v[28:35], v[178:181], v233, v233 op_sel_hi:[0,0,0]
	v_mfma_scale_f32_16x16x128_f8f6f4 v[94:97], v[158:165], v[28:35], v[182:185], v233, v233 op_sel_hi:[0,0,0]
	v_mfma_scale_f32_16x16x128_f8f6f4 v[90:93], v[150:157], v[36:43], v[186:189], v233, v233 op_sel_hi:[0,0,0]
	v_mfma_scale_f32_16x16x128_f8f6f4 v[86:89], v[158:165], v[36:43], v[190:193], v233, v233 op_sel_hi:[0,0,0]
	v_mfma_scale_f32_16x16x128_f8f6f4 v[82:85], v[150:157], v[44:51], v[194:197], v233, v233 op_sel_hi:[0,0,0]
	v_mfma_scale_f32_16x16x128_f8f6f4 v[78:81], v[158:165], v[44:51], v[198:201], v233, v233 op_sel_hi:[0,0,0]
	s_barrier
	s_mov_b32 m0, s35
	s_add_i32 s69, s68, 0x80
	ds_read_b128 v[20:23], v232 offset:49152
	ds_read_b128 v[24:27], v232 offset:50176
	ds_read_b128 v[166:169], v232 offset:51200
	ds_read_b128 v[170:173], v232 offset:52224
	ds_read_b128 v[174:177], v232 offset:53248
	ds_read_b128 v[178:181], v232 offset:54272
	ds_read_b128 v[182:185], v232 offset:55296
	ds_read_b128 v[186:189], v232 offset:56320
	buffer_load_dwordx4 v230, s[8:11], s69 offen lds
	s_add_i32 s69, s68, 0x10080
	s_mov_b32 m0, s36
	s_add_i32 s25, s25, 0x10080
	buffer_load_dwordx4 v230, s[8:11], s69 offen lds
	s_add_i32 s69, s68, 0x20080
	s_mov_b32 m0, s39
	s_add_i32 s68, s68, 0x30080
	buffer_load_dwordx4 v230, s[8:11], s69 offen lds
	s_mov_b32 m0, s40
	s_nop 0
	buffer_load_dwordx4 v230, s[8:11], s68 offen lds
	s_mov_b32 m0, s37
	s_nop 0
	buffer_load_dwordx4 v1, s[8:11], s67 offen lds
	s_mov_b32 m0, s38
	s_nop 0
	buffer_load_dwordx4 v1, s[8:11], s25 offen lds
	s_waitcnt vmcnt(8)
	s_waitcnt lgkmcnt(0)
	s_barrier
	s_waitcnt lgkmcnt(6)
	v_mfma_scale_f32_16x16x128_f8f6f4 v[74:77], v[2:9], v[20:27], v[74:77], v233, v233 op_sel_hi:[0,0,0]
	v_mfma_scale_f32_16x16x128_f8f6f4 v[70:73], v[12:19], v[20:27], v[70:73], v233, v233 op_sel_hi:[0,0,0]
	s_waitcnt lgkmcnt(4)
	v_mfma_scale_f32_16x16x128_f8f6f4 v[66:69], v[2:9], v[166:173], v[66:69], v233, v233 op_sel_hi:[0,0,0]
	v_mfma_scale_f32_16x16x128_f8f6f4 v[62:65], v[12:19], v[166:173], v[62:65], v233, v233 op_sel_hi:[0,0,0]
	s_waitcnt lgkmcnt(2)
	v_mfma_scale_f32_16x16x128_f8f6f4 v[58:61], v[2:9], v[174:181], v[58:61], v233, v233 op_sel_hi:[0,0,0]
	v_mfma_scale_f32_16x16x128_f8f6f4 v[54:57], v[12:19], v[174:181], v[54:57], v233, v233 op_sel_hi:[0,0,0]
	s_waitcnt lgkmcnt(0)
	v_mfma_scale_f32_16x16x128_f8f6f4 v[50:53], v[2:9], v[182:189], v[202:205], v233, v233 op_sel_hi:[0,0,0]
	v_mfma_scale_f32_16x16x128_f8f6f4 v[46:49], v[12:19], v[182:189], v[206:209], v233, v233 op_sel_hi:[0,0,0]
	v_mfma_scale_f32_16x16x128_f8f6f4 v[42:45], v[150:157], v[20:27], v[210:213], v233, v233 op_sel_hi:[0,0,0]
	v_mfma_scale_f32_16x16x128_f8f6f4 v[38:41], v[158:165], v[20:27], v[214:217], v233, v233 op_sel_hi:[0,0,0]
	v_mfma_scale_f32_16x16x128_f8f6f4 v[34:37], v[150:157], v[166:173], v[218:221], v233, v233 op_sel_hi:[0,0,0]
	v_mfma_scale_f32_16x16x128_f8f6f4 v[30:33], v[158:165], v[166:173], v[222:225], v233, v233 op_sel_hi:[0,0,0]
	v_mfma_scale_f32_16x16x128_f8f6f4 v[26:29], v[150:157], v[174:181], v[226:229], v233, v233 op_sel_hi:[0,0,0]
	v_mfma_scale_f32_16x16x128_f8f6f4 v[22:25], v[158:165], v[174:181], v[236:239], v233, v233 op_sel_hi:[0,0,0]
	v_mfma_scale_f32_16x16x128_f8f6f4 v[18:21], v[150:157], v[182:189], v[240:243], v233, v233 op_sel_hi:[0,0,0]
	v_mfma_scale_f32_16x16x128_f8f6f4 v[14:17], v[158:165], v[182:189], v[244:247], v233, v233 op_sel_hi:[0,0,0]
	s_barrier
	s_add_i32 s24, s24, 2
	s_addk_i32 s6, 0x100
	s_addk_i32 s7, 0x100
	s_cmp_gt_u32 s24, 5
	s_cbranch_scc0 .LBB0_1820
	s_and_b64 vcc, exec, s[20:21]
	s_cbranch_vccz .LBB0_1823
	s_barrier

.LBB0_2058:
	ds_read_b128 v[146:149], v138
	ds_read_b128 v[150:153], v138 offset:1024
	ds_read_b128 v[154:157], v138 offset:2048
	ds_read_b128 v[158:161], v138 offset:3072
	ds_read_b128 v[162:165], v139
	ds_read_b128 v[166:169], v139 offset:1024
	ds_read_b128 v[170:173], v139 offset:2048
	ds_read_b128 v[174:177], v139 offset:3072
	s_add_i32 s67, s6, 0xfffa0080
	s_cmp_eq_u32 s65, 12
	s_cselect_b32 s67, s63, s67
	s_cselect_b32 s69, s64, s7
	s_add_i32 s68, s67, 0x80
	s_add_i32 s70, s6, 0xfffe0000
	s_mov_b32 m0, s56
	ds_read_b128 v[178:181], v140
	ds_read_b128 v[182:185], v140 offset:1024
	ds_read_b128 v[186:189], v140 offset:2048
	ds_read_b128 v[190:193], v140 offset:3072
	ds_read_b128 v[194:197], v140 offset:4096
	ds_read_b128 v[198:201], v140 offset:5120
	ds_read_b128 v[202:205], v140 offset:6144
	ds_read_b128 v[206:209], v140 offset:7168
	buffer_load_dwordx4 v1, s[8:11], s70 offen lds
	s_mov_b32 m0, s57
	s_nop 0
	buffer_load_dwordx4 v1, s[8:11], s6 offen lds
	s_waitcnt vmcnt(8)
	s_waitcnt lgkmcnt(0)
	s_barrier
	s_waitcnt lgkmcnt(6)
	v_mfma_scale_f32_16x16x128_f8f6f4 v[126:129], v[146:153], v[178:185], v[126:129], v142, v141 op_sel_hi:[0,0,0]
	v_mfma_scale_f32_16x16x128_f8f6f4 v[122:125], v[154:161], v[178:185], v[122:125], v142, v141 op_sel_hi:[0,0,0]
	s_waitcnt lgkmcnt(4)
	v_mfma_scale_f32_16x16x128_f8f6f4 v[118:121], v[146:153], v[186:193], v[118:121], v142, v141 op_sel_hi:[0,0,0]
	v_mfma_scale_f32_16x16x128_f8f6f4 v[110:113], v[154:161], v[186:193], v[110:113], v142, v141 op_sel_hi:[0,0,0]
	s_waitcnt lgkmcnt(2)
	v_mfma_scale_f32_16x16x128_f8f6f4 v[102:105], v[146:153], v[194:201], v[102:105], v142, v141 op_sel_hi:[0,0,0]
	v_mfma_scale_f32_16x16x128_f8f6f4 v[130:133], v[154:161], v[194:201], v[94:97], v142, v141 op_sel_hi:[0,0,0]
	s_waitcnt lgkmcnt(0)
	v_mfma_scale_f32_16x16x128_f8f6f4 v[210:213], v[146:153], v[202:209], v[86:89], v142, v141 op_sel_hi:[0,0,0]
	v_mfma_scale_f32_16x16x128_f8f6f4 v[214:217], v[154:161], v[202:209], v[78:81], v142, v141 op_sel_hi:[0,0,0]
	v_mfma_scale_f32_16x16x128_f8f6f4 v[114:117], v[162:169], v[178:185], v[114:117], v142, v141 op_sel_hi:[0,0,0]
	v_mfma_scale_f32_16x16x128_f8f6f4 v[106:109], v[170:177], v[178:185], v[106:109], v142, v141 op_sel_hi:[0,0,0]
	v_mfma_scale_f32_16x16x128_f8f6f4 v[98:101], v[162:169], v[186:193], v[98:101], v142, v141 op_sel_hi:[0,0,0]
	v_mfma_scale_f32_16x16x128_f8f6f4 v[178:181], v[170:177], v[186:193], v[90:93], v142, v141 op_sel_hi:[0,0,0]
	v_mfma_scale_f32_16x16x128_f8f6f4 v[182:185], v[162:169], v[194:201], v[82:85], v142, v141 op_sel_hi:[0,0,0]
	v_mfma_scale_f32_16x16x128_f8f6f4 v[186:189], v[170:177], v[194:201], v[74:77], v142, v141 op_sel_hi:[0,0,0]
	v_mfma_scale_f32_16x16x128_f8f6f4 v[190:193], v[162:169], v[202:209], v[70:73], v142, v141 op_sel_hi:[0,0,0]
	v_mfma_scale_f32_16x16x128_f8f6f4 v[194:197], v[170:177], v[202:209], v[66:69], v142, v141 op_sel_hi:[0,0,0]
	s_barrier
	s_mov_b32 m0, s30
	s_nop 3
	ds_read_b128 v[66:69], v140 offset:16384
	ds_read_b128 v[70:73], v140 offset:17408
	ds_read_b128 v[74:77], v140 offset:18432
	ds_read_b128 v[78:81], v140 offset:19456
	ds_read_b128 v[82:85], v140 offset:20480
	ds_read_b128 v[86:89], v140 offset:21504
	ds_read_b128 v[90:93], v140 offset:22528
	ds_read_b128 v[94:97], v140 offset:23552
	buffer_load_dwordx4 v136, s[8:11], s69 offen lds
	s_add_i32 s70, s69, 0x20000
	s_mov_b32 m0, s31
	s_nop 0
	buffer_load_dwordx4 v136, s[8:11], s70 offen lds
	s_add_i32 s70, s69, 0x40000
	s_mov_b32 m0, s34
	s_nop 0
	buffer_load_dwordx4 v136, s[8:11], s70 offen lds
	s_add_i32 s70, s69, 0x60000
	s_mov_b32 m0, s35
	s_nop 0
	buffer_load_dwordx4 v136, s[8:11], s70 offen lds
	s_mov_b32 m0, s3
	s_add_i32 s70, s67, 0x20000
	buffer_load_dwordx4 v1, s[8:11], s67 offen lds
	s_mov_b32 m0, s36
	s_nop 0
	buffer_load_dwordx4 v1, s[8:11], s70 offen lds
	s_waitcnt vmcnt(8)
	s_waitcnt lgkmcnt(0)
	s_barrier
	s_waitcnt lgkmcnt(6)
	v_mfma_scale_f32_16x16x128_f8f6f4 v[62:65], v[146:153], v[66:73], v[62:65], v142, v141 op_sel_hi:[0,0,0]
	v_mfma_scale_f32_16x16x128_f8f6f4 v[58:61], v[154:161], v[66:73], v[58:61], v142, v141 op_sel_hi:[0,0,0]
	s_waitcnt lgkmcnt(4)
	v_mfma_scale_f32_16x16x128_f8f6f4 v[54:57], v[146:153], v[74:81], v[54:57], v142, v141 op_sel_hi:[0,0,0]
	v_mfma_scale_f32_16x16x128_f8f6f4 v[198:201], v[154:161], v[74:81], v[46:49], v142, v141 op_sel_hi:[0,0,0]
	s_waitcnt lgkmcnt(2)
	v_mfma_scale_f32_16x16x128_f8f6f4 v[202:205], v[146:153], v[82:89], v[38:41], v142, v141 op_sel_hi:[0,0,0]
	v_mfma_scale_f32_16x16x128_f8f6f4 v[206:209], v[154:161], v[82:89], v[30:33], v142, v141 op_sel_hi:[0,0,0]
	s_waitcnt lgkmcnt(0)
	v_mfma_scale_f32_16x16x128_f8f6f4 v[218:221], v[146:153], v[90:97], v[22:25], v142, v141 op_sel_hi:[0,0,0]
	v_mfma_scale_f32_16x16x128_f8f6f4 v[222:225], v[154:161], v[90:97], v[14:17], v142, v141 op_sel_hi:[0,0,0]
	v_mfma_scale_f32_16x16x128_f8f6f4 v[50:53], v[162:169], v[66:73], v[50:53], v142, v141 op_sel_hi:[0,0,0]
	v_mfma_scale_f32_16x16x128_f8f6f4 v[226:229], v[170:177], v[66:73], v[42:45], v142, v141 op_sel_hi:[0,0,0]
	v_mfma_scale_f32_16x16x128_f8f6f4 v[230:233], v[162:169], v[74:81], v[34:37], v142, v141 op_sel_hi:[0,0,0]
	v_mfma_scale_f32_16x16x128_f8f6f4 v[234:237], v[170:177], v[74:81], v[26:29], v142, v141 op_sel_hi:[0,0,0]
	v_mfma_scale_f32_16x16x128_f8f6f4 v[238:241], v[162:169], v[82:89], v[18:21], v142, v141 op_sel_hi:[0,0,0]
	v_mfma_scale_f32_16x16x128_f8f6f4 v[242:245], v[170:177], v[82:89], v[10:13], v142, v141 op_sel_hi:[0,0,0]
	v_mfma_scale_f32_16x16x128_f8f6f4 v[246:249], v[162:169], v[90:97], v[6:9], v142, v141 op_sel_hi:[0,0,0]
	v_mfma_scale_f32_16x16x128_f8f6f4 v[250:253], v[170:177], v[90:97], v[2:5], v142, v141 op_sel_hi:[0,0,0]
	s_barrier
	s_nop 4
	ds_read_b128 v[2:5], v143
	ds_read_b128 v[6:9], v143 offset:1024
	ds_read_b128 v[10:13], v143 offset:2048
	ds_read_b128 v[14:17], v143 offset:3072
	ds_read_b128 v[146:149], v144
	ds_read_b128 v[150:153], v144 offset:1024
	ds_read_b128 v[154:157], v144 offset:2048
	ds_read_b128 v[158:161], v144 offset:3072
	s_mov_b32 m0, s37
	s_add_i32 s70, s67, 0x40000
	ds_read_b128 v[18:21], v140 offset:32768
	ds_read_b128 v[22:25], v140 offset:33792
	ds_read_b128 v[26:29], v140 offset:34816
	ds_read_b128 v[30:33], v140 offset:35840
	ds_read_b128 v[34:37], v140 offset:36864
	ds_read_b128 v[38:41], v140 offset:37888
	ds_read_b128 v[42:45], v140 offset:38912
	ds_read_b128 v[46:49], v140 offset:39936
	buffer_load_dwordx4 v1, s[8:11], s70 offen lds
	s_add_i32 s70, s67, 0x60000
	s_mov_b32 m0, s38
	s_nop 0
	buffer_load_dwordx4 v1, s[8:11], s70 offen lds
	s_waitcnt vmcnt(8)
	s_waitcnt lgkmcnt(0)
	s_barrier
	s_waitcnt lgkmcnt(6)
	v_mfma_scale_f32_16x16x128_f8f6f4 v[126:129], v[2:9], v[18:25], v[126:129], v142, v141 op_sel_hi:[0,0,0]
	v_mfma_scale_f32_16x16x128_f8f6f4 v[122:125], v[10:17], v[18:25], v[122:125], v142, v141 op_sel_hi:[0,0,0]
	s_waitcnt lgkmcnt(4)
	v_mfma_scale_f32_16x16x128_f8f6f4 v[118:121], v[2:9], v[26:33], v[118:121], v142, v141 op_sel_hi:[0,0,0]
	v_mfma_scale_f32_16x16x128_f8f6f4 v[110:113], v[10:17], v[26:33], v[110:113], v142, v141 op_sel_hi:[0,0,0]
	s_waitcnt lgkmcnt(2)
	v_mfma_scale_f32_16x16x128_f8f6f4 v[102:105], v[2:9], v[34:41], v[102:105], v142, v141 op_sel_hi:[0,0,0]
	v_mfma_scale_f32_16x16x128_f8f6f4 v[94:97], v[10:17], v[34:41], v[130:133], v142, v141 op_sel_hi:[0,0,0]
	s_waitcnt lgkmcnt(0)
	v_mfma_scale_f32_16x16x128_f8f6f4 v[86:89], v[2:9], v[42:49], v[210:213], v142, v141 op_sel_hi:[0,0,0]
	v_mfma_scale_f32_16x16x128_f8f6f4 v[78:81], v[10:17], v[42:49], v[214:217], v142, v141 op_sel_hi:[0,0,0]
	v_mfma_scale_f32_16x16x128_f8f6f4 v[114:117], v[146:153], v[18:25], v[114:117], v142, v141 op_sel_hi:[0,0,0]
	v_mfma_scale_f32_16x16x128_f8f6f4 v[106:109], v[154:161], v[18:25], v[106:109], v142, v141 op_sel_hi:[0,0,0]
	v_mfma_scale_f32_16x16x128_f8f6f4 v[98:101], v[146:153], v[26:33], v[98:101], v142, v141 op_sel_hi:[0,0,0]
	v_mfma_scale_f32_16x16x128_f8f6f4 v[90:93], v[154:161], v[26:33], v[178:181], v142, v141 op_sel_hi:[0,0,0]
	v_mfma_scale_f32_16x16x128_f8f6f4 v[82:85], v[146:153], v[34:41], v[182:185], v142, v141 op_sel_hi:[0,0,0]
	v_mfma_scale_f32_16x16x128_f8f6f4 v[74:77], v[154:161], v[34:41], v[186:189], v142, v141 op_sel_hi:[0,0,0]
	v_mfma_scale_f32_16x16x128_f8f6f4 v[70:73], v[146:153], v[42:49], v[190:193], v142, v141 op_sel_hi:[0,0,0]
	v_mfma_scale_f32_16x16x128_f8f6f4 v[66:69], v[154:161], v[42:49], v[194:197], v142, v141 op_sel_hi:[0,0,0]
	s_barrier
	s_mov_b32 m0, s40
	s_add_i32 s70, s69, 0x80
	ds_read_b128 v[162:165], v140 offset:49152
	ds_read_b128 v[166:169], v140 offset:50176
	ds_read_b128 v[170:173], v140 offset:51200
	ds_read_b128 v[174:177], v140 offset:52224
	ds_read_b128 v[178:181], v140 offset:53248
	ds_read_b128 v[182:185], v140 offset:54272
	ds_read_b128 v[186:189], v140 offset:55296
	ds_read_b128 v[190:193], v140 offset:56320
	buffer_load_dwordx4 v136, s[8:11], s70 offen lds
	s_add_i32 s70, s69, 0x20080
	s_mov_b32 m0, s41
	s_add_i32 s67, s67, 0x20080
	buffer_load_dwordx4 v136, s[8:11], s70 offen lds
	s_add_i32 s70, s69, 0x40080
	s_mov_b32 m0, s49
	s_add_i32 s69, s69, 0x60080
	buffer_load_dwordx4 v136, s[8:11], s70 offen lds
	s_mov_b32 m0, s53
	s_nop 0
	buffer_load_dwordx4 v136, s[8:11], s69 offen lds
	s_mov_b32 m0, s42
	s_nop 0
	buffer_load_dwordx4 v1, s[8:11], s68 offen lds
	s_mov_b32 m0, s43
	s_nop 0
	buffer_load_dwordx4 v1, s[8:11], s67 offen lds
	s_waitcnt vmcnt(8)
	s_waitcnt lgkmcnt(0)
	s_barrier
	s_waitcnt lgkmcnt(6)
	v_mfma_scale_f32_16x16x128_f8f6f4 v[62:65], v[2:9], v[162:169], v[62:65], v142, v141 op_sel_hi:[0,0,0]
	v_mfma_scale_f32_16x16x128_f8f6f4 v[58:61], v[10:17], v[162:169], v[58:61], v142, v141 op_sel_hi:[0,0,0]
	s_waitcnt lgkmcnt(4)
	v_mfma_scale_f32_16x16x128_f8f6f4 v[54:57], v[2:9], v[170:177], v[54:57], v142, v141 op_sel_hi:[0,0,0]
	v_mfma_scale_f32_16x16x128_f8f6f4 v[46:49], v[10:17], v[170:177], v[198:201], v142, v141 op_sel_hi:[0,0,0]
	s_waitcnt lgkmcnt(2)
	v_mfma_scale_f32_16x16x128_f8f6f4 v[38:41], v[2:9], v[178:185], v[202:205], v142, v141 op_sel_hi:[0,0,0]
	v_mfma_scale_f32_16x16x128_f8f6f4 v[30:33], v[10:17], v[178:185], v[206:209], v142, v141 op_sel_hi:[0,0,0]
	s_waitcnt lgkmcnt(0)
	v_mfma_scale_f32_16x16x128_f8f6f4 v[22:25], v[2:9], v[186:193], v[218:221], v142, v141 op_sel_hi:[0,0,0]
	v_mfma_scale_f32_16x16x128_f8f6f4 v[14:17], v[10:17], v[186:193], v[222:225], v142, v141 op_sel_hi:[0,0,0]
	v_mfma_scale_f32_16x16x128_f8f6f4 v[50:53], v[146:153], v[162:169], v[50:53], v142, v141 op_sel_hi:[0,0,0]
	v_mfma_scale_f32_16x16x128_f8f6f4 v[42:45], v[154:161], v[162:169], v[226:229], v142, v141 op_sel_hi:[0,0,0]
	v_mfma_scale_f32_16x16x128_f8f6f4 v[34:37], v[146:153], v[170:177], v[230:233], v142, v141 op_sel_hi:[0,0,0]
	v_mfma_scale_f32_16x16x128_f8f6f4 v[26:29], v[154:161], v[170:177], v[234:237], v142, v141 op_sel_hi:[0,0,0]
	v_mfma_scale_f32_16x16x128_f8f6f4 v[18:21], v[146:153], v[178:185], v[238:241], v142, v141 op_sel_hi:[0,0,0]
	v_mfma_scale_f32_16x16x128_f8f6f4 v[10:13], v[154:161], v[178:185], v[242:245], v142, v141 op_sel_hi:[0,0,0]
	v_mfma_scale_f32_16x16x128_f8f6f4 v[6:9], v[146:153], v[186:193], v[246:249], v142, v141 op_sel_hi:[0,0,0]
	v_mfma_scale_f32_16x16x128_f8f6f4 v[2:5], v[154:161], v[186:193], v[250:253], v142, v141 op_sel_hi:[0,0,0]
	s_barrier
	s_add_i32 s65, s65, 2
	s_addk_i32 s6, 0x100
	s_addk_i32 s7, 0x100
	s_cmp_gt_u32 s65, 13
	s_cbranch_scc0 .LBB0_2058
	s_and_b64 vcc, exec, s[18:19]
	s_cbranch_vccz .LBB0_2061
	s_barrier

.LBB0_2336:
	ds_read_b128 v[106:109], v154
	ds_read_b128 v[110:113], v154 offset:1024
	ds_read_b128 v[138:141], v154 offset:2048
	ds_read_b128 v[142:145], v154 offset:3072
	ds_read_b128 v[162:165], v155
	ds_read_b128 v[166:169], v155 offset:1024
	ds_read_b128 v[170:173], v155 offset:2048
	ds_read_b128 v[174:177], v155 offset:3072
	s_add_i32 s65, s62, 0xfffa0080
	s_cmp_eq_u32 s64, 12
	s_cselect_b32 s65, s26, s65
	s_cselect_b32 s67, s27, s63
	s_add_i32 s66, s65, 0x80
	s_add_i32 s68, s62, 0xfffe0000
	s_mov_b32 m0, s53
	ds_read_b128 v[178:181], v156
	ds_read_b128 v[182:185], v156 offset:1024
	ds_read_b128 v[186:189], v156 offset:2048
	ds_read_b128 v[190:193], v156 offset:3072
	ds_read_b128 v[194:197], v156 offset:4096
	ds_read_b128 v[198:201], v156 offset:5120
	ds_read_b128 v[202:205], v156 offset:6144
	ds_read_b128 v[206:209], v156 offset:7168
	buffer_load_dwordx4 v1, s[8:11], s68 offen lds
	s_mov_b32 m0, s54
	s_nop 0
	buffer_load_dwordx4 v1, s[8:11], s62 offen lds
	s_waitcnt vmcnt(8)
	s_waitcnt lgkmcnt(0)
	s_barrier
	s_waitcnt lgkmcnt(6)
	v_mfma_scale_f32_16x16x128_f8f6f4 v[134:137], v[106:113], v[178:185], v[134:137], v158, v157 op_sel_hi:[0,0,0]
	v_mfma_scale_f32_16x16x128_f8f6f4 v[130:133], v[138:145], v[178:185], v[130:133], v158, v157 op_sel_hi:[0,0,0]
	s_waitcnt lgkmcnt(4)
	v_mfma_scale_f32_16x16x128_f8f6f4 v[126:129], v[106:113], v[186:193], v[126:129], v158, v157 op_sel_hi:[0,0,0]
	v_mfma_scale_f32_16x16x128_f8f6f4 v[122:125], v[138:145], v[186:193], v[122:125], v158, v157 op_sel_hi:[0,0,0]
	s_waitcnt lgkmcnt(2)
	v_mfma_scale_f32_16x16x128_f8f6f4 v[118:121], v[106:113], v[194:201], v[118:121], v158, v157 op_sel_hi:[0,0,0]
	v_mfma_scale_f32_16x16x128_f8f6f4 v[114:117], v[138:145], v[194:201], v[114:117], v158, v157 op_sel_hi:[0,0,0]
	s_waitcnt lgkmcnt(0)
	v_mfma_scale_f32_16x16x128_f8f6f4 v[102:105], v[106:113], v[202:209], v[102:105], v158, v157 op_sel_hi:[0,0,0]
	v_mfma_scale_f32_16x16x128_f8f6f4 v[98:101], v[138:145], v[202:209], v[98:101], v158, v157 op_sel_hi:[0,0,0]
	v_mfma_scale_f32_16x16x128_f8f6f4 v[146:149], v[162:169], v[178:185], v[62:65], v158, v157 op_sel_hi:[0,0,0]
	v_mfma_scale_f32_16x16x128_f8f6f4 v[178:181], v[170:177], v[178:185], v[58:61], v158, v157 op_sel_hi:[0,0,0]
	v_mfma_scale_f32_16x16x128_f8f6f4 v[182:185], v[162:169], v[186:193], v[54:57], v158, v157 op_sel_hi:[0,0,0]
	v_mfma_scale_f32_16x16x128_f8f6f4 v[186:189], v[170:177], v[186:193], v[50:53], v158, v157 op_sel_hi:[0,0,0]
	v_mfma_scale_f32_16x16x128_f8f6f4 v[190:193], v[162:169], v[194:201], v[46:49], v158, v157 op_sel_hi:[0,0,0]
	v_mfma_scale_f32_16x16x128_f8f6f4 v[194:197], v[170:177], v[194:201], v[42:45], v158, v157 op_sel_hi:[0,0,0]
	v_mfma_scale_f32_16x16x128_f8f6f4 v[198:201], v[162:169], v[202:209], v[38:41], v158, v157 op_sel_hi:[0,0,0]
	v_mfma_scale_f32_16x16x128_f8f6f4 v[202:205], v[170:177], v[202:209], v[34:37], v158, v157 op_sel_hi:[0,0,0]
	s_barrier
	s_mov_b32 m0, s23
	s_nop 3
	ds_read_b128 v[34:37], v156 offset:16384
	ds_read_b128 v[38:41], v156 offset:17408
	ds_read_b128 v[42:45], v156 offset:18432
	ds_read_b128 v[46:49], v156 offset:19456
	ds_read_b128 v[50:53], v156 offset:20480
	ds_read_b128 v[54:57], v156 offset:21504
	ds_read_b128 v[58:61], v156 offset:22528
	ds_read_b128 v[62:65], v156 offset:23552
	buffer_load_dwordx4 v152, s[8:11], s67 offen lds
	s_add_i32 s68, s67, 0x20000
	s_mov_b32 m0, s28
	s_nop 0
	buffer_load_dwordx4 v152, s[8:11], s68 offen lds
	s_add_i32 s68, s67, 0x40000
	s_mov_b32 m0, s29
	s_nop 0
	buffer_load_dwordx4 v152, s[8:11], s68 offen lds
	s_add_i32 s68, s67, 0x60000
	s_mov_b32 m0, s30
	s_nop 0
	buffer_load_dwordx4 v152, s[8:11], s68 offen lds
	s_mov_b32 m0, s3
	s_add_i32 s68, s65, 0x20000
	buffer_load_dwordx4 v1, s[8:11], s65 offen lds
	s_mov_b32 m0, s31
	s_nop 0
	buffer_load_dwordx4 v1, s[8:11], s68 offen lds
	s_waitcnt vmcnt(8)
	s_waitcnt lgkmcnt(0)
	s_barrier
	s_waitcnt lgkmcnt(6)
	v_mfma_scale_f32_16x16x128_f8f6f4 v[94:97], v[106:113], v[34:41], v[94:97], v158, v157 op_sel_hi:[0,0,0]
	v_mfma_scale_f32_16x16x128_f8f6f4 v[90:93], v[138:145], v[34:41], v[90:93], v158, v157 op_sel_hi:[0,0,0]
	s_waitcnt lgkmcnt(4)
	v_mfma_scale_f32_16x16x128_f8f6f4 v[86:89], v[106:113], v[42:49], v[86:89], v158, v157 op_sel_hi:[0,0,0]
	v_mfma_scale_f32_16x16x128_f8f6f4 v[82:85], v[138:145], v[42:49], v[82:85], v158, v157 op_sel_hi:[0,0,0]
	s_waitcnt lgkmcnt(2)
	v_mfma_scale_f32_16x16x128_f8f6f4 v[78:81], v[106:113], v[50:57], v[78:81], v158, v157 op_sel_hi:[0,0,0]
	v_mfma_scale_f32_16x16x128_f8f6f4 v[74:77], v[138:145], v[50:57], v[74:77], v158, v157 op_sel_hi:[0,0,0]
	s_waitcnt lgkmcnt(0)
	v_mfma_scale_f32_16x16x128_f8f6f4 v[206:209], v[106:113], v[58:65], v[70:73], v158, v157 op_sel_hi:[0,0,0]
	v_mfma_scale_f32_16x16x128_f8f6f4 v[210:213], v[138:145], v[58:65], v[66:69], v158, v157 op_sel_hi:[0,0,0]
	v_mfma_scale_f32_16x16x128_f8f6f4 v[214:217], v[162:169], v[34:41], v[30:33], v158, v157 op_sel_hi:[0,0,0]
	v_mfma_scale_f32_16x16x128_f8f6f4 v[218:221], v[170:177], v[34:41], v[26:29], v158, v157 op_sel_hi:[0,0,0]
	v_mfma_scale_f32_16x16x128_f8f6f4 v[222:225], v[162:169], v[42:49], v[22:25], v158, v157 op_sel_hi:[0,0,0]
	v_mfma_scale_f32_16x16x128_f8f6f4 v[226:229], v[170:177], v[42:49], v[18:21], v158, v157 op_sel_hi:[0,0,0]
	v_mfma_scale_f32_16x16x128_f8f6f4 v[230:233], v[162:169], v[50:57], v[14:17], v158, v157 op_sel_hi:[0,0,0]
	v_mfma_scale_f32_16x16x128_f8f6f4 v[234:237], v[170:177], v[50:57], v[10:13], v158, v157 op_sel_hi:[0,0,0]
	v_mfma_scale_f32_16x16x128_f8f6f4 v[238:241], v[162:169], v[58:65], v[6:9], v158, v157 op_sel_hi:[0,0,0]
	v_mfma_scale_f32_16x16x128_f8f6f4 v[242:245], v[170:177], v[58:65], v[2:5], v158, v157 op_sel_hi:[0,0,0]
	s_barrier
	s_nop 4
	ds_read_b128 v[2:5], v159
	ds_read_b128 v[6:9], v159 offset:1024
	ds_read_b128 v[10:13], v159 offset:2048
	ds_read_b128 v[14:17], v159 offset:3072
	ds_read_b128 v[106:109], v160
	ds_read_b128 v[110:113], v160 offset:1024
	ds_read_b128 v[138:141], v160 offset:2048
	ds_read_b128 v[142:145], v160 offset:3072
	s_mov_b32 m0, s34
	s_add_i32 s68, s65, 0x40000
	ds_read_b128 v[18:21], v156 offset:32768
	ds_read_b128 v[22:25], v156 offset:33792
	ds_read_b128 v[26:29], v156 offset:34816
	ds_read_b128 v[30:33], v156 offset:35840
	ds_read_b128 v[34:37], v156 offset:36864
	ds_read_b128 v[38:41], v156 offset:37888
	ds_read_b128 v[66:69], v156 offset:38912
	ds_read_b128 v[70:73], v156 offset:39936
	buffer_load_dwordx4 v1, s[8:11], s68 offen lds
	s_add_i32 s68, s65, 0x60000
	s_mov_b32 m0, s35
	s_nop 0
	buffer_load_dwordx4 v1, s[8:11], s68 offen lds
	s_waitcnt vmcnt(8)
	s_waitcnt lgkmcnt(0)
	s_barrier
	s_waitcnt lgkmcnt(6)
	v_mfma_scale_f32_16x16x128_f8f6f4 v[134:137], v[2:9], v[18:25], v[134:137], v158, v157 op_sel_hi:[0,0,0]
	v_mfma_scale_f32_16x16x128_f8f6f4 v[130:133], v[10:17], v[18:25], v[130:133], v158, v157 op_sel_hi:[0,0,0]
	s_waitcnt lgkmcnt(4)
	v_mfma_scale_f32_16x16x128_f8f6f4 v[126:129], v[2:9], v[26:33], v[126:129], v158, v157 op_sel_hi:[0,0,0]
	v_mfma_scale_f32_16x16x128_f8f6f4 v[122:125], v[10:17], v[26:33], v[122:125], v158, v157 op_sel_hi:[0,0,0]
	s_waitcnt lgkmcnt(2)
	v_mfma_scale_f32_16x16x128_f8f6f4 v[118:121], v[2:9], v[34:41], v[118:121], v158, v157 op_sel_hi:[0,0,0]
	v_mfma_scale_f32_16x16x128_f8f6f4 v[114:117], v[10:17], v[34:41], v[114:117], v158, v157 op_sel_hi:[0,0,0]
	s_waitcnt lgkmcnt(0)
	v_mfma_scale_f32_16x16x128_f8f6f4 v[102:105], v[2:9], v[66:73], v[102:105], v158, v157 op_sel_hi:[0,0,0]
	v_mfma_scale_f32_16x16x128_f8f6f4 v[98:101], v[10:17], v[66:73], v[98:101], v158, v157 op_sel_hi:[0,0,0]
	v_mfma_scale_f32_16x16x128_f8f6f4 v[62:65], v[106:113], v[18:25], v[146:149], v158, v157 op_sel_hi:[0,0,0]
	v_mfma_scale_f32_16x16x128_f8f6f4 v[58:61], v[138:145], v[18:25], v[178:181], v158, v157 op_sel_hi:[0,0,0]
	v_mfma_scale_f32_16x16x128_f8f6f4 v[54:57], v[106:113], v[26:33], v[182:185], v158, v157 op_sel_hi:[0,0,0]
	v_mfma_scale_f32_16x16x128_f8f6f4 v[50:53], v[138:145], v[26:33], v[186:189], v158, v157 op_sel_hi:[0,0,0]
	v_mfma_scale_f32_16x16x128_f8f6f4 v[46:49], v[106:113], v[34:41], v[190:193], v158, v157 op_sel_hi:[0,0,0]
	v_mfma_scale_f32_16x16x128_f8f6f4 v[42:45], v[138:145], v[34:41], v[194:197], v158, v157 op_sel_hi:[0,0,0]
	v_mfma_scale_f32_16x16x128_f8f6f4 v[38:41], v[106:113], v[66:73], v[198:201], v158, v157 op_sel_hi:[0,0,0]
	v_mfma_scale_f32_16x16x128_f8f6f4 v[34:37], v[138:145], v[66:73], v[202:205], v158, v157 op_sel_hi:[0,0,0]
	s_barrier
	s_mov_b32 m0, s36
	s_add_i32 s68, s67, 0x80
	ds_read_b128 v[18:21], v156 offset:49152
	ds_read_b128 v[22:25], v156 offset:50176
	ds_read_b128 v[162:165], v156 offset:51200
	ds_read_b128 v[166:169], v156 offset:52224
	ds_read_b128 v[170:173], v156 offset:53248
	ds_read_b128 v[174:177], v156 offset:54272
	ds_read_b128 v[178:181], v156 offset:55296
	ds_read_b128 v[182:185], v156 offset:56320
	buffer_load_dwordx4 v152, s[8:11], s68 offen lds
	s_add_i32 s68, s67, 0x20080
	s_mov_b32 m0, s37
	s_add_i32 s65, s65, 0x20080
	buffer_load_dwordx4 v152, s[8:11], s68 offen lds
	s_add_i32 s68, s67, 0x40080
	s_mov_b32 m0, s40
	s_add_i32 s67, s67, 0x60080
	buffer_load_dwordx4 v152, s[8:11], s68 offen lds
	s_mov_b32 m0, s41
	s_nop 0
	buffer_load_dwordx4 v152, s[8:11], s67 offen lds
	s_mov_b32 m0, s38
	s_nop 0
	buffer_load_dwordx4 v1, s[8:11], s66 offen lds
	s_mov_b32 m0, s39
	s_nop 0
	buffer_load_dwordx4 v1, s[8:11], s65 offen lds
	s_waitcnt vmcnt(8)
	s_waitcnt lgkmcnt(0)
	s_barrier
	s_waitcnt lgkmcnt(6)
	v_mfma_scale_f32_16x16x128_f8f6f4 v[94:97], v[2:9], v[18:25], v[94:97], v158, v157 op_sel_hi:[0,0,0]
	v_mfma_scale_f32_16x16x128_f8f6f4 v[90:93], v[10:17], v[18:25], v[90:93], v158, v157 op_sel_hi:[0,0,0]
	s_waitcnt lgkmcnt(4)
	v_mfma_scale_f32_16x16x128_f8f6f4 v[86:89], v[2:9], v[162:169], v[86:89], v158, v157 op_sel_hi:[0,0,0]
	v_mfma_scale_f32_16x16x128_f8f6f4 v[82:85], v[10:17], v[162:169], v[82:85], v158, v157 op_sel_hi:[0,0,0]
	s_waitcnt lgkmcnt(2)
	v_mfma_scale_f32_16x16x128_f8f6f4 v[78:81], v[2:9], v[170:177], v[78:81], v158, v157 op_sel_hi:[0,0,0]
	v_mfma_scale_f32_16x16x128_f8f6f4 v[74:77], v[10:17], v[170:177], v[74:77], v158, v157 op_sel_hi:[0,0,0]
	s_waitcnt lgkmcnt(0)
	v_mfma_scale_f32_16x16x128_f8f6f4 v[70:73], v[2:9], v[178:185], v[206:209], v158, v157 op_sel_hi:[0,0,0]
	v_mfma_scale_f32_16x16x128_f8f6f4 v[66:69], v[10:17], v[178:185], v[210:213], v158, v157 op_sel_hi:[0,0,0]
	v_mfma_scale_f32_16x16x128_f8f6f4 v[30:33], v[106:113], v[18:25], v[214:217], v158, v157 op_sel_hi:[0,0,0]
	v_mfma_scale_f32_16x16x128_f8f6f4 v[26:29], v[138:145], v[18:25], v[218:221], v158, v157 op_sel_hi:[0,0,0]
	v_mfma_scale_f32_16x16x128_f8f6f4 v[22:25], v[106:113], v[162:169], v[222:225], v158, v157 op_sel_hi:[0,0,0]
	v_mfma_scale_f32_16x16x128_f8f6f4 v[18:21], v[138:145], v[162:169], v[226:229], v158, v157 op_sel_hi:[0,0,0]
	v_mfma_scale_f32_16x16x128_f8f6f4 v[14:17], v[106:113], v[170:177], v[230:233], v158, v157 op_sel_hi:[0,0,0]
	v_mfma_scale_f32_16x16x128_f8f6f4 v[10:13], v[138:145], v[170:177], v[234:237], v158, v157 op_sel_hi:[0,0,0]
	v_mfma_scale_f32_16x16x128_f8f6f4 v[6:9], v[106:113], v[178:185], v[238:241], v158, v157 op_sel_hi:[0,0,0]
	v_mfma_scale_f32_16x16x128_f8f6f4 v[2:5], v[138:145], v[178:185], v[242:245], v158, v157 op_sel_hi:[0,0,0]
	s_barrier
	s_add_i32 s64, s64, 2
	s_addk_i32 s62, 0x100
	s_addk_i32 s63, 0x100
	s_cmp_gt_u32 s64, 13
	s_cbranch_scc0 .LBB0_2336
	s_and_b64 vcc, exec, s[20:21]
	s_cbranch_vccz .LBB0_2339
	s_barrier

.LBB0_2426:
	ds_read_b128 v[130:133], v167
	ds_read_b128 v[134:137], v167 offset:1024
	ds_read_b128 v[138:141], v167 offset:2048
	ds_read_b128 v[142:145], v167 offset:3072
	ds_read_b128 v[148:151], v168
	ds_read_b128 v[152:155], v168 offset:1024
	ds_read_b128 v[156:159], v168 offset:2048
	ds_read_b128 v[160:163], v168 offset:3072
	s_add_i32 s30, s8, 0xfffa0080
	s_cmp_eq_u32 s11, 12
	s_cselect_b32 s30, s66, s30
	s_cselect_b32 s68, s67, s9
	s_add_i32 s31, s30, 0x80
	s_add_i32 s69, s8, 0xfffe0000
	s_mov_b32 m0, s58
	ds_read_b128 v[176:179], v169
	ds_read_b128 v[180:183], v169 offset:1024
	ds_read_b128 v[184:187], v169 offset:2048
	ds_read_b128 v[188:191], v169 offset:3072
	ds_read_b128 v[192:195], v169 offset:4096
	ds_read_b128 v[196:199], v169 offset:5120
	ds_read_b128 v[200:203], v169 offset:6144
	ds_read_b128 v[204:207], v169 offset:7168
	buffer_load_dwordx4 v1, s[12:15], s69 offen lds
	s_mov_b32 m0, s59
	s_nop 0
	buffer_load_dwordx4 v1, s[12:15], s8 offen lds
	s_waitcnt vmcnt(8)
	s_waitcnt lgkmcnt(0)
	s_barrier
	s_waitcnt lgkmcnt(6)
	v_mfma_scale_f32_16x16x128_f8f6f4 v[126:129], v[130:137], v[176:183], v[126:129], v171, v170 op_sel_hi:[0,0,0]
	v_mfma_scale_f32_16x16x128_f8f6f4 v[122:125], v[138:145], v[176:183], v[122:125], v171, v170 op_sel_hi:[0,0,0]
	s_waitcnt lgkmcnt(4)
	v_mfma_scale_f32_16x16x128_f8f6f4 v[118:121], v[130:137], v[184:191], v[118:121], v171, v170 op_sel_hi:[0,0,0]
	v_mfma_scale_f32_16x16x128_f8f6f4 v[114:117], v[138:145], v[184:191], v[114:117], v171, v170 op_sel_hi:[0,0,0]
	s_waitcnt lgkmcnt(2)
	v_mfma_scale_f32_16x16x128_f8f6f4 v[110:113], v[130:137], v[192:199], v[110:113], v171, v170 op_sel_hi:[0,0,0]
	v_mfma_scale_f32_16x16x128_f8f6f4 v[106:109], v[138:145], v[192:199], v[106:109], v171, v170 op_sel_hi:[0,0,0]
	s_waitcnt lgkmcnt(0)
	v_mfma_scale_f32_16x16x128_f8f6f4 v[102:105], v[130:137], v[200:207], v[102:105], v171, v170 op_sel_hi:[0,0,0]
	v_mfma_scale_f32_16x16x128_f8f6f4 v[98:101], v[138:145], v[200:207], v[98:101], v171, v170 op_sel_hi:[0,0,0]
	v_mfma_scale_f32_16x16x128_f8f6f4 v[208:211], v[148:155], v[176:183], v[94:97], v171, v170 op_sel_hi:[0,0,0]
	v_mfma_scale_f32_16x16x128_f8f6f4 v[176:179], v[156:163], v[176:183], v[90:93], v171, v170 op_sel_hi:[0,0,0]
	v_mfma_scale_f32_16x16x128_f8f6f4 v[180:183], v[148:155], v[184:191], v[86:89], v171, v170 op_sel_hi:[0,0,0]
	v_mfma_scale_f32_16x16x128_f8f6f4 v[184:187], v[156:163], v[184:191], v[82:85], v171, v170 op_sel_hi:[0,0,0]
	v_mfma_scale_f32_16x16x128_f8f6f4 v[188:191], v[148:155], v[192:199], v[78:81], v171, v170 op_sel_hi:[0,0,0]
	v_mfma_scale_f32_16x16x128_f8f6f4 v[192:195], v[156:163], v[192:199], v[74:77], v171, v170 op_sel_hi:[0,0,0]
	v_mfma_scale_f32_16x16x128_f8f6f4 v[196:199], v[148:155], v[200:207], v[70:73], v171, v170 op_sel_hi:[0,0,0]
	v_mfma_scale_f32_16x16x128_f8f6f4 v[200:203], v[156:163], v[200:207], v[66:69], v171, v170 op_sel_hi:[0,0,0]
	s_barrier
	s_mov_b32 m0, s34
	s_nop 3
	ds_read_b128 v[66:69], v169 offset:16384
	ds_read_b128 v[70:73], v169 offset:17408
	ds_read_b128 v[74:77], v169 offset:18432
	ds_read_b128 v[78:81], v169 offset:19456
	ds_read_b128 v[82:85], v169 offset:20480
	ds_read_b128 v[86:89], v169 offset:21504
	ds_read_b128 v[90:93], v169 offset:22528
	ds_read_b128 v[94:97], v169 offset:23552
	buffer_load_dwordx4 v165, s[12:15], s68 offen lds
	s_add_i32 s69, s68, 0x20000
	s_mov_b32 m0, s35
	s_nop 0
	buffer_load_dwordx4 v165, s[12:15], s69 offen lds
	s_add_i32 s69, s68, 0x40000
	s_mov_b32 m0, s36
	s_nop 0
	buffer_load_dwordx4 v165, s[12:15], s69 offen lds
	s_add_i32 s69, s68, 0x60000
	s_mov_b32 m0, s37
	s_nop 0
	buffer_load_dwordx4 v165, s[12:15], s69 offen lds
	s_mov_b32 m0, s3
	s_add_i32 s69, s30, 0x20000
	buffer_load_dwordx4 v1, s[12:15], s30 offen lds
	s_mov_b32 m0, s38
	s_nop 0
	buffer_load_dwordx4 v1, s[12:15], s69 offen lds
	s_waitcnt vmcnt(8)
	s_waitcnt lgkmcnt(0)
	s_barrier
	s_waitcnt lgkmcnt(6)
	v_mfma_scale_f32_16x16x128_f8f6f4 v[62:65], v[130:137], v[66:73], v[62:65], v171, v170 op_sel_hi:[0,0,0]
	v_mfma_scale_f32_16x16x128_f8f6f4 v[58:61], v[138:145], v[66:73], v[58:61], v171, v170 op_sel_hi:[0,0,0]
	s_waitcnt lgkmcnt(4)
	v_mfma_scale_f32_16x16x128_f8f6f4 v[54:57], v[130:137], v[74:81], v[54:57], v171, v170 op_sel_hi:[0,0,0]
	v_mfma_scale_f32_16x16x128_f8f6f4 v[50:53], v[138:145], v[74:81], v[50:53], v171, v170 op_sel_hi:[0,0,0]
	s_waitcnt lgkmcnt(2)
	v_mfma_scale_f32_16x16x128_f8f6f4 v[204:207], v[130:137], v[82:89], v[46:49], v171, v170 op_sel_hi:[0,0,0]
	v_mfma_scale_f32_16x16x128_f8f6f4 v[212:215], v[138:145], v[82:89], v[42:45], v171, v170 op_sel_hi:[0,0,0]
	s_waitcnt lgkmcnt(0)
	v_mfma_scale_f32_16x16x128_f8f6f4 v[216:219], v[130:137], v[90:97], v[38:41], v171, v170 op_sel_hi:[0,0,0]
	v_mfma_scale_f32_16x16x128_f8f6f4 v[220:223], v[138:145], v[90:97], v[34:37], v171, v170 op_sel_hi:[0,0,0]
	v_mfma_scale_f32_16x16x128_f8f6f4 v[224:227], v[148:155], v[66:73], v[30:33], v171, v170 op_sel_hi:[0,0,0]
	v_mfma_scale_f32_16x16x128_f8f6f4 v[228:231], v[156:163], v[66:73], v[26:29], v171, v170 op_sel_hi:[0,0,0]
	v_mfma_scale_f32_16x16x128_f8f6f4 v[232:235], v[148:155], v[74:81], v[22:25], v171, v170 op_sel_hi:[0,0,0]
	v_mfma_scale_f32_16x16x128_f8f6f4 v[236:239], v[156:163], v[74:81], v[18:21], v171, v170 op_sel_hi:[0,0,0]
	v_mfma_scale_f32_16x16x128_f8f6f4 v[240:243], v[148:155], v[82:89], v[14:17], v171, v170 op_sel_hi:[0,0,0]
	v_mfma_scale_f32_16x16x128_f8f6f4 v[244:247], v[156:163], v[82:89], v[10:13], v171, v170 op_sel_hi:[0,0,0]
	v_mfma_scale_f32_16x16x128_f8f6f4 v[248:251], v[148:155], v[90:97], v[6:9], v171, v170 op_sel_hi:[0,0,0]
	v_mfma_scale_f32_16x16x128_f8f6f4 v[252:255], v[156:163], v[90:97], v[2:5], v171, v170 op_sel_hi:[0,0,0]
	s_barrier
	s_nop 4
	ds_read_b128 v[2:5], v172
	ds_read_b128 v[6:9], v172 offset:1024
	ds_read_b128 v[10:13], v172 offset:2048
	ds_read_b128 v[14:17], v172 offset:3072
	ds_read_b128 v[130:133], v173
	ds_read_b128 v[134:137], v173 offset:1024
	ds_read_b128 v[138:141], v173 offset:2048
	ds_read_b128 v[142:145], v173 offset:3072
	s_mov_b32 m0, s39
	s_add_i32 s69, s30, 0x40000
	ds_read_b128 v[18:21], v169 offset:32768
	ds_read_b128 v[22:25], v169 offset:33792
	ds_read_b128 v[26:29], v169 offset:34816
	ds_read_b128 v[30:33], v169 offset:35840
	ds_read_b128 v[34:37], v169 offset:36864
	ds_read_b128 v[38:41], v169 offset:37888
	ds_read_b128 v[42:45], v169 offset:38912
	ds_read_b128 v[46:49], v169 offset:39936
	buffer_load_dwordx4 v1, s[12:15], s69 offen lds
	s_add_i32 s69, s30, 0x60000
	s_mov_b32 m0, s40
	s_nop 0
	buffer_load_dwordx4 v1, s[12:15], s69 offen lds
	s_waitcnt vmcnt(8)
	s_waitcnt lgkmcnt(0)
	s_barrier
	s_waitcnt lgkmcnt(6)
	v_mfma_scale_f32_16x16x128_f8f6f4 v[126:129], v[2:9], v[18:25], v[126:129], v171, v170 op_sel_hi:[0,0,0]
	v_mfma_scale_f32_16x16x128_f8f6f4 v[122:125], v[10:17], v[18:25], v[122:125], v171, v170 op_sel_hi:[0,0,0]
	s_waitcnt lgkmcnt(4)
	v_mfma_scale_f32_16x16x128_f8f6f4 v[118:121], v[2:9], v[26:33], v[118:121], v171, v170 op_sel_hi:[0,0,0]
	v_mfma_scale_f32_16x16x128_f8f6f4 v[114:117], v[10:17], v[26:33], v[114:117], v171, v170 op_sel_hi:[0,0,0]
	s_waitcnt lgkmcnt(2)
	v_mfma_scale_f32_16x16x128_f8f6f4 v[110:113], v[2:9], v[34:41], v[110:113], v171, v170 op_sel_hi:[0,0,0]
	v_mfma_scale_f32_16x16x128_f8f6f4 v[106:109], v[10:17], v[34:41], v[106:109], v171, v170 op_sel_hi:[0,0,0]
	s_waitcnt lgkmcnt(0)
	v_mfma_scale_f32_16x16x128_f8f6f4 v[102:105], v[2:9], v[42:49], v[102:105], v171, v170 op_sel_hi:[0,0,0]
	v_mfma_scale_f32_16x16x128_f8f6f4 v[98:101], v[10:17], v[42:49], v[98:101], v171, v170 op_sel_hi:[0,0,0]
	v_mfma_scale_f32_16x16x128_f8f6f4 v[94:97], v[130:137], v[18:25], v[208:211], v171, v170 op_sel_hi:[0,0,0]
	v_mfma_scale_f32_16x16x128_f8f6f4 v[90:93], v[138:145], v[18:25], v[176:179], v171, v170 op_sel_hi:[0,0,0]
	v_mfma_scale_f32_16x16x128_f8f6f4 v[86:89], v[130:137], v[26:33], v[180:183], v171, v170 op_sel_hi:[0,0,0]
	v_mfma_scale_f32_16x16x128_f8f6f4 v[82:85], v[138:145], v[26:33], v[184:187], v171, v170 op_sel_hi:[0,0,0]
	v_mfma_scale_f32_16x16x128_f8f6f4 v[78:81], v[130:137], v[34:41], v[188:191], v171, v170 op_sel_hi:[0,0,0]
	v_mfma_scale_f32_16x16x128_f8f6f4 v[74:77], v[138:145], v[34:41], v[192:195], v171, v170 op_sel_hi:[0,0,0]
	v_mfma_scale_f32_16x16x128_f8f6f4 v[70:73], v[130:137], v[42:49], v[196:199], v171, v170 op_sel_hi:[0,0,0]
	v_mfma_scale_f32_16x16x128_f8f6f4 v[66:69], v[138:145], v[42:49], v[200:203], v171, v170 op_sel_hi:[0,0,0]
	s_barrier
	s_mov_b32 m0, s42
	s_add_i32 s69, s68, 0x80
	ds_read_b128 v[18:21], v169 offset:49152
	ds_read_b128 v[22:25], v169 offset:50176
	ds_read_b128 v[148:151], v169 offset:51200
	ds_read_b128 v[152:155], v169 offset:52224
	ds_read_b128 v[156:159], v169 offset:53248
	ds_read_b128 v[160:163], v169 offset:54272
	ds_read_b128 v[176:179], v169 offset:55296
	ds_read_b128 v[180:183], v169 offset:56320
	buffer_load_dwordx4 v165, s[12:15], s69 offen lds
	s_add_i32 s69, s68, 0x20080
	s_mov_b32 m0, s43
	s_add_i32 s30, s30, 0x20080
	buffer_load_dwordx4 v165, s[12:15], s69 offen lds
	s_add_i32 s69, s68, 0x40080
	s_mov_b32 m0, s54
	s_add_i32 s68, s68, 0x60080
	buffer_load_dwordx4 v165, s[12:15], s69 offen lds
	s_mov_b32 m0, s55
	s_nop 0
	buffer_load_dwordx4 v165, s[12:15], s68 offen lds
	s_mov_b32 m0, s49
	s_nop 0
	buffer_load_dwordx4 v1, s[12:15], s31 offen lds
	s_mov_b32 m0, s53
	s_nop 0
	buffer_load_dwordx4 v1, s[12:15], s30 offen lds
	s_waitcnt vmcnt(8)
	s_waitcnt lgkmcnt(0)
	s_barrier
	s_waitcnt lgkmcnt(6)
	v_mfma_scale_f32_16x16x128_f8f6f4 v[62:65], v[2:9], v[18:25], v[62:65], v171, v170 op_sel_hi:[0,0,0]
	v_mfma_scale_f32_16x16x128_f8f6f4 v[58:61], v[10:17], v[18:25], v[58:61], v171, v170 op_sel_hi:[0,0,0]
	s_waitcnt lgkmcnt(4)
	v_mfma_scale_f32_16x16x128_f8f6f4 v[54:57], v[2:9], v[148:155], v[54:57], v171, v170 op_sel_hi:[0,0,0]
	v_mfma_scale_f32_16x16x128_f8f6f4 v[50:53], v[10:17], v[148:155], v[50:53], v171, v170 op_sel_hi:[0,0,0]
	s_waitcnt lgkmcnt(2)
	v_mfma_scale_f32_16x16x128_f8f6f4 v[46:49], v[2:9], v[156:163], v[204:207], v171, v170 op_sel_hi:[0,0,0]
	v_mfma_scale_f32_16x16x128_f8f6f4 v[42:45], v[10:17], v[156:163], v[212:215], v171, v170 op_sel_hi:[0,0,0]
	s_waitcnt lgkmcnt(0)
	v_mfma_scale_f32_16x16x128_f8f6f4 v[38:41], v[2:9], v[176:183], v[216:219], v171, v170 op_sel_hi:[0,0,0]
	v_mfma_scale_f32_16x16x128_f8f6f4 v[34:37], v[10:17], v[176:183], v[220:223], v171, v170 op_sel_hi:[0,0,0]
	v_mfma_scale_f32_16x16x128_f8f6f4 v[30:33], v[130:137], v[18:25], v[224:227], v171, v170 op_sel_hi:[0,0,0]
	v_mfma_scale_f32_16x16x128_f8f6f4 v[26:29], v[138:145], v[18:25], v[228:231], v171, v170 op_sel_hi:[0,0,0]
	v_mfma_scale_f32_16x16x128_f8f6f4 v[22:25], v[130:137], v[148:155], v[232:235], v171, v170 op_sel_hi:[0,0,0]
	v_mfma_scale_f32_16x16x128_f8f6f4 v[18:21], v[138:145], v[148:155], v[236:239], v171, v170 op_sel_hi:[0,0,0]
	v_mfma_scale_f32_16x16x128_f8f6f4 v[14:17], v[130:137], v[156:163], v[240:243], v171, v170 op_sel_hi:[0,0,0]
	v_mfma_scale_f32_16x16x128_f8f6f4 v[10:13], v[138:145], v[156:163], v[244:247], v171, v170 op_sel_hi:[0,0,0]
	v_mfma_scale_f32_16x16x128_f8f6f4 v[6:9], v[130:137], v[176:183], v[248:251], v171, v170 op_sel_hi:[0,0,0]
	v_mfma_scale_f32_16x16x128_f8f6f4 v[2:5], v[138:145], v[176:183], v[252:255], v171, v170 op_sel_hi:[0,0,0]
	s_barrier
	s_add_i32 s11, s11, 2
	s_addk_i32 s8, 0x100
	s_addk_i32 s9, 0x100
	s_cmp_gt_u32 s11, 13
	s_cbranch_scc0 .LBB0_2426
	s_and_b64 vcc, exec, s[28:29]
	s_cbranch_vccz .LBB0_2429
	s_barrier
